# speedup vs baseline: 1.0250x; 1.0250x over previous
.LBB2_78:
	s_endpgm
	.p2align	8

_Z8moe_gemmILi2048ELi1024ELb0EEvPKDF16_S1_PKfPDF16_PfPKiS7_:
	s_load_dwordx2 s[14:15], s[0:1], 0x28
	s_load_dword s20, s[0:1], 0x38
	v_lshrrev_b32_e32 v1, 6, v0
	v_and_b32_e32 v2, 63, v0
	v_readfirstlane_b32 s58, v1
	s_waitcnt lgkmcnt(0)
	s_load_dword s24, s[14:15], 0x0
	s_load_dword s25, s[14:15], 0x80
	s_load_dword s26, s[14:15], 0x100
	s_load_dword s27, s[14:15], 0x180
	s_load_dword s28, s[14:15], 0x200
	s_load_dword s29, s[14:15], 0x280
	s_load_dword s30, s[14:15], 0x300
	s_load_dword s31, s[14:15], 0x380
	s_waitcnt lgkmcnt(0)
	s_mov_b32 s21, 0
	s_add_i32 s22, s24, 0x9f
	s_mul_hi_i32 s22, s22, 0x66666667
	s_lshr_b32 s23, s22, 31
	s_ashr_i32 s32, s22, 6
	s_add_i32 s32, s32, s23
	s_add_i32 s22, s24, 15
	s_lshr_b32 s22, s22, 4
	s_add_i32 s22, s22, s32
	s_add_i32 s22, s22, -1
	s_mov_b32 s40, 0
	s_cmp_eq_u32 s32, 0
	s_cbranch_scc1 .Lg2_dx1
	s_mov_b32 s23, s32
.Lg2_dv1:
	s_cmp_le_u32 s23, s22
	s_cbranch_scc0 .Lg2_dx1
	s_add_i32 s40, s40, 1
	s_add_i32 s23, s23, s32
	s_branch .Lg2_dv1
.Lg2_dx1:
	s_add_i32 s21, s21, s32
	s_add_i32 s22, s25, 0x9f
	s_mul_hi_i32 s22, s22, 0x66666667
	s_lshr_b32 s23, s22, 31
	s_ashr_i32 s33, s22, 6
	s_add_i32 s33, s33, s23
	s_add_i32 s22, s25, 15
	s_lshr_b32 s22, s22, 4
	s_add_i32 s22, s22, s33
	s_add_i32 s22, s22, -1
	s_mov_b32 s41, 0
	s_cmp_eq_u32 s33, 0
	s_cbranch_scc1 .Lg2_dx2
	s_mov_b32 s23, s33
.Lg2_dv2:
	s_cmp_le_u32 s23, s22
	s_cbranch_scc0 .Lg2_dx2
	s_add_i32 s41, s41, 1
	s_add_i32 s23, s23, s33
	s_branch .Lg2_dv2
.Lg2_dx2:
	s_add_i32 s21, s21, s33
	s_add_i32 s22, s26, 0x9f
	s_mul_hi_i32 s22, s22, 0x66666667
	s_lshr_b32 s23, s22, 31
	s_ashr_i32 s34, s22, 6
	s_add_i32 s34, s34, s23
	s_add_i32 s22, s26, 15
	s_lshr_b32 s22, s22, 4
	s_add_i32 s22, s22, s34
	s_add_i32 s22, s22, -1
	s_mov_b32 s42, 0
	s_cmp_eq_u32 s34, 0
	s_cbranch_scc1 .Lg2_dx3
	s_mov_b32 s23, s34
.Lg2_dv3:
	s_cmp_le_u32 s23, s22
	s_cbranch_scc0 .Lg2_dx3
	s_add_i32 s42, s42, 1
	s_add_i32 s23, s23, s34
	s_branch .Lg2_dv3
.Lg2_dx3:
	s_add_i32 s21, s21, s34
	s_add_i32 s22, s27, 0x9f
	s_mul_hi_i32 s22, s22, 0x66666667
	s_lshr_b32 s23, s22, 31
	s_ashr_i32 s35, s22, 6
	s_add_i32 s35, s35, s23
	s_add_i32 s22, s27, 15
	s_lshr_b32 s22, s22, 4
	s_add_i32 s22, s22, s35
	s_add_i32 s22, s22, -1
	s_mov_b32 s43, 0
	s_cmp_eq_u32 s35, 0
	s_cbranch_scc1 .Lg2_dx4
	s_mov_b32 s23, s35
.Lg2_dv4:
	s_cmp_le_u32 s23, s22
	s_cbranch_scc0 .Lg2_dx4
	s_add_i32 s43, s43, 1
	s_add_i32 s23, s23, s35
	s_branch .Lg2_dv4
.Lg2_dx4:
	s_add_i32 s21, s21, s35
	s_add_i32 s22, s28, 0x9f
	s_mul_hi_i32 s22, s22, 0x66666667
	s_lshr_b32 s23, s22, 31
	s_ashr_i32 s36, s22, 6
	s_add_i32 s36, s36, s23
	s_add_i32 s22, s28, 15
	s_lshr_b32 s22, s22, 4
	s_add_i32 s22, s22, s36
	s_add_i32 s22, s22, -1
	s_mov_b32 s44, 0
	s_cmp_eq_u32 s36, 0
	s_cbranch_scc1 .Lg2_dx5
	s_mov_b32 s23, s36
.Lg2_dv5:
	s_cmp_le_u32 s23, s22
	s_cbranch_scc0 .Lg2_dx5
	s_add_i32 s44, s44, 1
	s_add_i32 s23, s23, s36
	s_branch .Lg2_dv5
.Lg2_dx5:
	s_add_i32 s21, s21, s36
	s_add_i32 s22, s29, 0x9f
	s_mul_hi_i32 s22, s22, 0x66666667
	s_lshr_b32 s23, s22, 31
	s_ashr_i32 s37, s22, 6
	s_add_i32 s37, s37, s23
	s_add_i32 s22, s29, 15
	s_lshr_b32 s22, s22, 4
	s_add_i32 s22, s22, s37
	s_add_i32 s22, s22, -1
	s_mov_b32 s45, 0
	s_cmp_eq_u32 s37, 0
	s_cbranch_scc1 .Lg2_dx6
	s_mov_b32 s23, s37
.Lg2_dv6:
	s_cmp_le_u32 s23, s22
	s_cbranch_scc0 .Lg2_dx6
	s_add_i32 s45, s45, 1
	s_add_i32 s23, s23, s37
	s_branch .Lg2_dv6
.Lg2_dx6:
	s_add_i32 s21, s21, s37
	s_add_i32 s22, s30, 0x9f
	s_mul_hi_i32 s22, s22, 0x66666667
	s_lshr_b32 s23, s22, 31
	s_ashr_i32 s38, s22, 6
	s_add_i32 s38, s38, s23
	s_add_i32 s22, s30, 15
	s_lshr_b32 s22, s22, 4
	s_add_i32 s22, s22, s38
	s_add_i32 s22, s22, -1
	s_mov_b32 s46, 0
	s_cmp_eq_u32 s38, 0
	s_cbranch_scc1 .Lg2_dx7
	s_mov_b32 s23, s38
.Lg2_dv7:
	s_cmp_le_u32 s23, s22
	s_cbranch_scc0 .Lg2_dx7
	s_add_i32 s46, s46, 1
	s_add_i32 s23, s23, s38
	s_branch .Lg2_dv7
.Lg2_dx7:
	s_add_i32 s21, s21, s38
	s_add_i32 s22, s31, 0x9f
	s_mul_hi_i32 s22, s22, 0x66666667
	s_lshr_b32 s23, s22, 31
	s_ashr_i32 s39, s22, 6
	s_add_i32 s39, s39, s23
	s_add_i32 s22, s31, 15
	s_lshr_b32 s22, s22, 4
	s_add_i32 s22, s22, s39
	s_add_i32 s22, s22, -1
	s_mov_b32 s47, 0
	s_cmp_eq_u32 s39, 0
	s_cbranch_scc1 .Lg2_dx8
	s_mov_b32 s23, s39
.Lg2_dv8:
	s_cmp_le_u32 s23, s22
	s_cbranch_scc0 .Lg2_dx8
	s_add_i32 s47, s47, 1
	s_add_i32 s23, s23, s39
	s_branch .Lg2_dv8
.Lg2_dx8:
	s_add_i32 s21, s21, s39
	s_lshl_b32 s21, s21, 2
	s_and_b32 s22, s2, 7
	s_mul_i32 s23, s21, s22
	s_ashr_i32 s18, s23, 3
	s_add_i32 s23, s23, s21
	s_ashr_i32 s19, s23, 3
	s_lshr_b32 s22, s2, 3
	s_add_i32 s18, s18, s22
	s_lshr_b32 s20, s20, 3
	s_cmp_ge_i32 s18, s19
	s_cbranch_scc1 .Lg2_end
	s_load_dwordx4 s[4:7], s[0:1], 0x0
	s_load_dwordx4 s[8:11], s[0:1], 0x10
	s_load_dwordx2 s[12:13], s[0:1], 0x20
	s_load_dwordx2 s[16:17], s[0:1], 0x30
	s_lshr_b32 s59, s58, 1
	s_and_b32 s60, s58, 1
	s_lshl_b32 s70, s58, 10
	s_movk_i32 s69, 0x1080
	v_and_b32_e32 v3, 15, v2
	v_lshrrev_b32_e32 v4, 4, v2
	v_lshrrev_b32_e32 v5, 3, v0
	v_bfe_u32 v8, v5, 1, 3
	v_bfe_u32 v9, v5, 4, 1
	v_xor_b32_e32 v8, v8, v9
	v_and_b32_e32 v9, 7, v0
	v_xor_b32_e32 v8, v8, v9
	v_lshlrev_b32_e32 v6, 4, v8
	v_bfe_u32 v8, v0, 4, 2
	v_bfe_u32 v9, v0, 7, 1
	v_lshl_or_b32 v8, v9, 2, v8
	v_lshlrev_b32_e32 v8, 1, v8
	v_and_b32_e32 v9, 15, v0
	v_xor_b32_e32 v8, v8, v9
	v_lshlrev_b32_e32 v8, 4, v8
	v_lshrrev_b32_e32 v9, 4, v0
	v_lshlrev_b32_e32 v9, 11, v9
	v_add_u32_e32 v7, v8, v9
	v_bfe_u32 v8, v2, 2, 2
	v_and_b32_e32 v9, 1, v4
	v_lshl_or_b32 v56, v9, 2, v8
	v_lshl_add_u32 v8, v4, 3, v8
	v_lshlrev_b32_e32 v8, 8, v8
	v_and_b32_e32 v9, 3, v2
	v_lshlrev_b32_e32 v9, 3, v9
	v_add_u32_e32 v8, v8, v9
	s_lshl_b32 s74, s60, 14
	s_add_u32 s74, s74, 0x5000
	v_add_u32_e32 v8, s74, v8
	v_xor_b32_e32 v9, 0, v56
	v_lshl_add_u32 v40, v9, 5, v8
	v_add_u32_e32 v48, 0xd000, v40
	v_xor_b32_e32 v9, 1, v56
	v_lshl_add_u32 v41, v9, 5, v8
	v_add_u32_e32 v49, 0xd000, v41
	v_xor_b32_e32 v9, 2, v56
	v_lshl_add_u32 v42, v9, 5, v8
	v_add_u32_e32 v50, 0xd000, v42
	v_xor_b32_e32 v9, 3, v56
	v_lshl_add_u32 v43, v9, 5, v8
	v_add_u32_e32 v51, 0xd000, v43
	v_xor_b32_e32 v9, 4, v56
	v_lshl_add_u32 v44, v9, 5, v8
	v_add_u32_e32 v52, 0xd000, v44
	v_xor_b32_e32 v9, 5, v56
	v_lshl_add_u32 v45, v9, 5, v8
	v_add_u32_e32 v53, 0xd000, v45
	v_xor_b32_e32 v9, 6, v56
	v_lshl_add_u32 v46, v9, 5, v8
	v_add_u32_e32 v54, 0xd000, v46
	v_xor_b32_e32 v9, 7, v56
	v_lshl_add_u32 v47, v9, 5, v8
	v_add_u32_e32 v55, 0xd000, v47
	s_waitcnt lgkmcnt(0)
.Lg2_tile:
	s_mov_b32 s71, s18
	s_mov_b32 s72, 0
	s_lshl_b32 s22, s32, 2
	s_cmp_lt_i32 s71, s22
	s_cbranch_scc0 .Lg2_ne0
	s_mov_b32 s48, 0
	s_mov_b32 s49, s24
	s_mov_b32 s50, s40
	s_mov_b32 s68, s32
	s_branch .Lg2_dec
.Lg2_ne0:
	s_sub_i32 s71, s71, s22
	s_mul_i32 s22, s32, s40
	s_lshl_b32 s22, s22, 4
	s_add_i32 s72, s72, s22
	s_lshl_b32 s22, s33, 2
	s_cmp_lt_i32 s71, s22
	s_cbranch_scc0 .Lg2_ne1
	s_mov_b32 s48, 1
	s_mov_b32 s49, s25
	s_mov_b32 s50, s41
	s_mov_b32 s68, s33
	s_branch .Lg2_dec
.Lg2_ne1:
	s_sub_i32 s71, s71, s22
	s_mul_i32 s22, s33, s41
	s_lshl_b32 s22, s22, 4
	s_add_i32 s72, s72, s22
	s_lshl_b32 s22, s34, 2
	s_cmp_lt_i32 s71, s22
	s_cbranch_scc0 .Lg2_ne2
	s_mov_b32 s48, 2
	s_mov_b32 s49, s26
	s_mov_b32 s50, s42
	s_mov_b32 s68, s34
	s_branch .Lg2_dec
.Lg2_ne2:
	s_sub_i32 s71, s71, s22
	s_mul_i32 s22, s34, s42
	s_lshl_b32 s22, s22, 4
	s_add_i32 s72, s72, s22
	s_lshl_b32 s22, s35, 2
	s_cmp_lt_i32 s71, s22
	s_cbranch_scc0 .Lg2_ne3
	s_mov_b32 s48, 3
	s_mov_b32 s49, s27
	s_mov_b32 s50, s43
	s_mov_b32 s68, s35
	s_branch .Lg2_dec
.Lg2_ne3:
	s_sub_i32 s71, s71, s22
	s_mul_i32 s22, s35, s43
	s_lshl_b32 s22, s22, 4
	s_add_i32 s72, s72, s22
	s_lshl_b32 s22, s36, 2
	s_cmp_lt_i32 s71, s22
	s_cbranch_scc0 .Lg2_ne4
	s_mov_b32 s48, 4
	s_mov_b32 s49, s28
	s_mov_b32 s50, s44
	s_mov_b32 s68, s36
	s_branch .Lg2_dec
.Lg2_ne4:
	s_sub_i32 s71, s71, s22
	s_mul_i32 s22, s36, s44
	s_lshl_b32 s22, s22, 4
	s_add_i32 s72, s72, s22
	s_lshl_b32 s22, s37, 2
	s_cmp_lt_i32 s71, s22
	s_cbranch_scc0 .Lg2_ne5
	s_mov_b32 s48, 5
	s_mov_b32 s49, s29
	s_mov_b32 s50, s45
	s_mov_b32 s68, s37
	s_branch .Lg2_dec
.Lg2_ne5:
	s_sub_i32 s71, s71, s22
	s_mul_i32 s22, s37, s45
	s_lshl_b32 s22, s22, 4
	s_add_i32 s72, s72, s22
	s_lshl_b32 s22, s38, 2
	s_cmp_lt_i32 s71, s22
	s_cbranch_scc0 .Lg2_ne6
	s_mov_b32 s48, 6
	s_mov_b32 s49, s30
	s_mov_b32 s50, s46
	s_mov_b32 s68, s38
	s_branch .Lg2_dec
.Lg2_ne6:
	s_sub_i32 s71, s71, s22
	s_mul_i32 s22, s38, s46
	s_lshl_b32 s22, s22, 4
	s_add_i32 s72, s72, s22
	s_lshl_b32 s22, s39, 2
	s_cmp_lt_i32 s71, s22
	s_cbranch_scc0 .Lg2_ne7
	s_mov_b32 s48, 7
	s_mov_b32 s49, s31
	s_mov_b32 s50, s47
	s_mov_b32 s68, s39
	s_branch .Lg2_dec
.Lg2_ne7:
	s_sub_i32 s71, s71, s22
	s_mul_i32 s22, s39, s47
	s_lshl_b32 s22, s22, 4
	s_add_i32 s72, s72, s22
	s_branch .Lg2_end
.Lg2_dec:
	s_mov_b32 s53, s72
	s_mov_b32 s51, 0
.Lg2_ntl:
	s_cmp_ge_i32 s71, s68
	s_cbranch_scc0 .Lg2_ntd
	s_sub_i32 s71, s71, s68
	s_add_i32 s51, s51, 1
	s_branch .Lg2_ntl
.Lg2_ntd:
	s_mov_b32 s52, s71
	s_lshl_b32 s57, s51, 8
	s_mul_i32 s54, s52, s50
	s_lshl_b32 s54, s54, 4
	s_add_i32 s55, s53, s54
	s_add_i32 s56, s50, 1
	s_lshr_b32 s56, s56, 1
	s_sub_i32 s22, s50, s56
	s_cmp_eq_u32 s59, 0
	s_cselect_b32 s61, 0, s56
	s_cselect_b32 s62, s56, s22
	s_barrier
	s_mul_i32 s22, s48, 0x400
	s_add_i32 s22, s22, s57
	s_lshl_b32 s23, s60, 7
	s_add_i32 s22, s22, s23
	v_lshl_add_u32 v8, v4, 2, s22
	v_lshlrev_b32_e32 v8, 2, v8
	global_load_dwordx4 v[200:203], v8, s[8:9] offset:0
	global_load_dwordx4 v[204:207], v8, s[8:9] offset:64
	global_load_dwordx4 v[208:211], v8, s[8:9] offset:128
	global_load_dwordx4 v[212:215], v8, s[8:9] offset:192
	global_load_dwordx4 v[216:219], v8, s[8:9] offset:256
	global_load_dwordx4 v[220:223], v8, s[8:9] offset:320
	global_load_dwordx4 v[224:227], v8, s[8:9] offset:384
	global_load_dwordx4 v[228:231], v8, s[8:9] offset:448
	s_lshl_b32 s22, s61, 4
	s_add_i32 s22, s22, s54
	v_add_u32_e32 v241, s22, v3
	s_lshl_b32 s23, s48, 13
	v_add_u32_e32 v8, 0, v241
	v_cmp_gt_u32_e32 vcc, s49, v8
	s_nop 1
	v_cndmask_b32_e32 v8, 0, v8, vcc
	v_add_lshl_u32 v8, v8, s23, 2
	global_load_dword v232, v8, s[16:17]
	v_add_u32_e32 v8, 16, v241
	v_cmp_gt_u32_e32 vcc, s49, v8
	s_nop 1
	v_cndmask_b32_e32 v8, 0, v8, vcc
	v_add_lshl_u32 v8, v8, s23, 2
	global_load_dword v233, v8, s[16:17]
	v_add_u32_e32 v8, 32, v241
	v_cmp_gt_u32_e32 vcc, s49, v8
	s_nop 1
	v_cndmask_b32_e32 v8, 0, v8, vcc
	v_add_lshl_u32 v8, v8, s23, 2
	global_load_dword v234, v8, s[16:17]
	v_add_u32_e32 v8, 48, v241
	v_cmp_gt_u32_e32 vcc, s49, v8
	s_nop 1
	v_cndmask_b32_e32 v8, 0, v8, vcc
	v_add_lshl_u32 v8, v8, s23, 2
	global_load_dword v235, v8, s[16:17]
	v_add_u32_e32 v8, 64, v241
	v_cmp_gt_u32_e32 vcc, s49, v8
	s_nop 1
	v_cndmask_b32_e32 v8, 0, v8, vcc
	v_add_lshl_u32 v8, v8, s23, 2
	global_load_dword v236, v8, s[16:17]
	v_add_u32_e32 v8, s55, v5
	v_mad_u32_u24 v10, v8, s69, v6
	v_add_u32_e32 v11, 0x21000, v10
	v_add_u32_e32 v12, 0x42000, v10
	v_add_u32_e32 v13, 0x63000, v10
	v_add_u32_e32 v14, 0x84000, v10
	s_lshl_b32 s22, s57, 1
	v_add_u32_e32 v20, s22, v7
	v_add_u32_e32 v21, 0x8000, v20
	v_add_u32_e32 v22, 0x10000, v20
	v_add_u32_e32 v23, 0x18000, v20
	v_add_u32_e32 v24, 0x100, v20
	v_add_u32_e32 v25, 0x8100, v20
	v_add_u32_e32 v26, 0x10100, v20
	v_add_u32_e32 v27, 0x18100, v20
	s_lshl_b32 s22, s61, 4
	v_add_u32_e32 v8, s22, v3
	v_lshlrev_b32_e32 v8, 7, v8
	v_lshrrev_b32_e32 v9, 1, v3
	v_xor_b32_e32 v9, v9, v4
	s_and_b32 s22, s61, 1
	v_xor_b32_e32 v9, s22, v9
	v_xor_b32_e32 v56, 0, v9
	v_lshl_add_u32 v30, v56, 4, v8
	v_add_u32_e32 v34, 0xd000, v30
	v_xor_b32_e32 v56, 1, v9
	v_lshl_add_u32 v31, v56, 4, v8
	v_add_u32_e32 v35, 0xd000, v31
	v_xor_b32_e32 v56, 4, v9
	v_lshl_add_u32 v32, v56, 4, v8
	v_add_u32_e32 v36, 0xd000, v32
	v_xor_b32_e32 v56, 5, v9
	v_lshl_add_u32 v33, v56, 4, v8
	v_add_u32_e32 v37, 0xd000, v33
	s_mov_b64 s[64:65], s[4:5]
	s_mul_i32 s22, s48, 0x400000
	s_add_u32 s66, s6, s22
	s_addc_u32 s67, s7, 0
	v_accvgpr_write_b32 a0, 0
	v_accvgpr_write_b32 a1, 0
	v_accvgpr_write_b32 a2, 0
	v_accvgpr_write_b32 a3, 0
	v_accvgpr_write_b32 a4, 0
	v_accvgpr_write_b32 a5, 0
	v_accvgpr_write_b32 a6, 0
	v_accvgpr_write_b32 a7, 0
	v_accvgpr_write_b32 a8, 0
	v_accvgpr_write_b32 a9, 0
	v_accvgpr_write_b32 a10, 0
	v_accvgpr_write_b32 a11, 0
	v_accvgpr_write_b32 a12, 0
	v_accvgpr_write_b32 a13, 0
	v_accvgpr_write_b32 a14, 0
	v_accvgpr_write_b32 a15, 0
	v_accvgpr_write_b32 a16, 0
	v_accvgpr_write_b32 a17, 0
	v_accvgpr_write_b32 a18, 0
	v_accvgpr_write_b32 a19, 0
	v_accvgpr_write_b32 a20, 0
	v_accvgpr_write_b32 a21, 0
	v_accvgpr_write_b32 a22, 0
	v_accvgpr_write_b32 a23, 0
	v_accvgpr_write_b32 a24, 0
	v_accvgpr_write_b32 a25, 0
	v_accvgpr_write_b32 a26, 0
	v_accvgpr_write_b32 a27, 0
	v_accvgpr_write_b32 a28, 0
	v_accvgpr_write_b32 a29, 0
	v_accvgpr_write_b32 a30, 0
	v_accvgpr_write_b32 a31, 0
	v_accvgpr_write_b32 a32, 0
	v_accvgpr_write_b32 a33, 0
	v_accvgpr_write_b32 a34, 0
	v_accvgpr_write_b32 a35, 0
	v_accvgpr_write_b32 a36, 0
	v_accvgpr_write_b32 a37, 0
	v_accvgpr_write_b32 a38, 0
	v_accvgpr_write_b32 a39, 0
	v_accvgpr_write_b32 a40, 0
	v_accvgpr_write_b32 a41, 0
	v_accvgpr_write_b32 a42, 0
	v_accvgpr_write_b32 a43, 0
	v_accvgpr_write_b32 a44, 0
	v_accvgpr_write_b32 a45, 0
	v_accvgpr_write_b32 a46, 0
	v_accvgpr_write_b32 a47, 0
	v_accvgpr_write_b32 a48, 0
	v_accvgpr_write_b32 a49, 0
	v_accvgpr_write_b32 a50, 0
	v_accvgpr_write_b32 a51, 0
	v_accvgpr_write_b32 a52, 0
	v_accvgpr_write_b32 a53, 0
	v_accvgpr_write_b32 a54, 0
	v_accvgpr_write_b32 a55, 0
	v_accvgpr_write_b32 a56, 0
	v_accvgpr_write_b32 a57, 0
	v_accvgpr_write_b32 a58, 0
	v_accvgpr_write_b32 a59, 0
	v_accvgpr_write_b32 a60, 0
	v_accvgpr_write_b32 a61, 0
	v_accvgpr_write_b32 a62, 0
	v_accvgpr_write_b32 a63, 0
	v_accvgpr_write_b32 a64, 0
	v_accvgpr_write_b32 a65, 0
	v_accvgpr_write_b32 a66, 0
	v_accvgpr_write_b32 a67, 0
	v_accvgpr_write_b32 a68, 0
	v_accvgpr_write_b32 a69, 0
	v_accvgpr_write_b32 a70, 0
	v_accvgpr_write_b32 a71, 0
	v_accvgpr_write_b32 a72, 0
	v_accvgpr_write_b32 a73, 0
	v_accvgpr_write_b32 a74, 0
	v_accvgpr_write_b32 a75, 0
	v_accvgpr_write_b32 a76, 0
	v_accvgpr_write_b32 a77, 0
	v_accvgpr_write_b32 a78, 0
	v_accvgpr_write_b32 a79, 0
	v_accvgpr_write_b32 a80, 0
	v_accvgpr_write_b32 a81, 0
	v_accvgpr_write_b32 a82, 0
	v_accvgpr_write_b32 a83, 0
	v_accvgpr_write_b32 a84, 0
	v_accvgpr_write_b32 a85, 0
	v_accvgpr_write_b32 a86, 0
	v_accvgpr_write_b32 a87, 0
	v_accvgpr_write_b32 a88, 0
	v_accvgpr_write_b32 a89, 0
	v_accvgpr_write_b32 a90, 0
	v_accvgpr_write_b32 a91, 0
	v_accvgpr_write_b32 a92, 0
	v_accvgpr_write_b32 a93, 0
	v_accvgpr_write_b32 a94, 0
	v_accvgpr_write_b32 a95, 0
	v_accvgpr_write_b32 a96, 0
	v_accvgpr_write_b32 a97, 0
	v_accvgpr_write_b32 a98, 0
	v_accvgpr_write_b32 a99, 0
	v_accvgpr_write_b32 a100, 0
	v_accvgpr_write_b32 a101, 0
	v_accvgpr_write_b32 a102, 0
	v_accvgpr_write_b32 a103, 0
	v_accvgpr_write_b32 a104, 0
	v_accvgpr_write_b32 a105, 0
	v_accvgpr_write_b32 a106, 0
	v_accvgpr_write_b32 a107, 0
	v_accvgpr_write_b32 a108, 0
	v_accvgpr_write_b32 a109, 0
	v_accvgpr_write_b32 a110, 0
	v_accvgpr_write_b32 a111, 0
	v_accvgpr_write_b32 a112, 0
	v_accvgpr_write_b32 a113, 0
	v_accvgpr_write_b32 a114, 0
	v_accvgpr_write_b32 a115, 0
	v_accvgpr_write_b32 a116, 0
	v_accvgpr_write_b32 a117, 0
	v_accvgpr_write_b32 a118, 0
	v_accvgpr_write_b32 a119, 0
	v_accvgpr_write_b32 a120, 0
	v_accvgpr_write_b32 a121, 0
	v_accvgpr_write_b32 a122, 0
	v_accvgpr_write_b32 a123, 0
	v_accvgpr_write_b32 a124, 0
	v_accvgpr_write_b32 a125, 0
	v_accvgpr_write_b32 a126, 0
	v_accvgpr_write_b32 a127, 0
	v_accvgpr_write_b32 a128, 0
	v_accvgpr_write_b32 a129, 0
	v_accvgpr_write_b32 a130, 0
	v_accvgpr_write_b32 a131, 0
	v_accvgpr_write_b32 a132, 0
	v_accvgpr_write_b32 a133, 0
	v_accvgpr_write_b32 a134, 0
	v_accvgpr_write_b32 a135, 0
	v_accvgpr_write_b32 a136, 0
	v_accvgpr_write_b32 a137, 0
	v_accvgpr_write_b32 a138, 0
	v_accvgpr_write_b32 a139, 0
	v_accvgpr_write_b32 a140, 0
	v_accvgpr_write_b32 a141, 0
	v_accvgpr_write_b32 a142, 0
	v_accvgpr_write_b32 a143, 0
	v_accvgpr_write_b32 a144, 0
	v_accvgpr_write_b32 a145, 0
	v_accvgpr_write_b32 a146, 0
	v_accvgpr_write_b32 a147, 0
	v_accvgpr_write_b32 a148, 0
	v_accvgpr_write_b32 a149, 0
	v_accvgpr_write_b32 a150, 0
	v_accvgpr_write_b32 a151, 0
	v_accvgpr_write_b32 a152, 0
	v_accvgpr_write_b32 a153, 0
	v_accvgpr_write_b32 a154, 0
	v_accvgpr_write_b32 a155, 0
	v_accvgpr_write_b32 a156, 0
	v_accvgpr_write_b32 a157, 0
	v_accvgpr_write_b32 a158, 0
	v_accvgpr_write_b32 a159, 0
	s_mov_b32 s80, 0
	s_mov_b32 s81, 0xd000
	s_mov_b32 s82, 0x1a000
	s_add_u32 s83, s70, s80
	s_add_u32 m0, s83, 0x0
	s_nop 0
	global_load_lds_dwordx4 v10, s[64:65]
	s_add_u32 m0, s83, 0x1000
	s_nop 0
	global_load_lds_dwordx4 v11, s[64:65]
	s_add_u32 m0, s83, 0x2000
	s_nop 0
	global_load_lds_dwordx4 v12, s[64:65]
	s_add_u32 m0, s83, 0x3000
	s_nop 0
	global_load_lds_dwordx4 v13, s[64:65]
	s_add_u32 m0, s83, 0x4000
	s_nop 0
	global_load_lds_dwordx4 v14, s[64:65]
	s_add_u32 m0, s83, 0x5000
	s_nop 0
	global_load_lds_dwordx4 v20, s[66:67]
	s_add_u32 m0, s83, 0x6000
	s_nop 0
	global_load_lds_dwordx4 v21, s[66:67]
	s_add_u32 m0, s83, 0x7000
	s_nop 0
	global_load_lds_dwordx4 v22, s[66:67]
	s_add_u32 m0, s83, 0x8000
	s_nop 0
	global_load_lds_dwordx4 v23, s[66:67]
	s_add_u32 m0, s83, 0x9000
	s_nop 0
	global_load_lds_dwordx4 v24, s[66:67]
	s_add_u32 m0, s83, 0xa000
	s_nop 0
	global_load_lds_dwordx4 v25, s[66:67]
	s_add_u32 m0, s83, 0xb000
	s_nop 0
	global_load_lds_dwordx4 v26, s[66:67]
	s_add_u32 m0, s83, 0xc000
	s_nop 0
	global_load_lds_dwordx4 v27, s[66:67]
	s_add_u32 s64, s64, 0x80
	s_addc_u32 s65, s65, 0
	s_add_u32 s66, s66, 0x20000
	s_addc_u32 s67, s67, 0
	s_add_u32 s83, s70, s81
	s_add_u32 m0, s83, 0x0
	s_nop 0
	global_load_lds_dwordx4 v10, s[64:65]
	s_add_u32 m0, s83, 0x1000
	s_nop 0
	global_load_lds_dwordx4 v11, s[64:65]
	s_add_u32 m0, s83, 0x2000
	s_nop 0
	global_load_lds_dwordx4 v12, s[64:65]
	s_add_u32 m0, s83, 0x3000
	s_nop 0
	global_load_lds_dwordx4 v13, s[64:65]
	s_add_u32 m0, s83, 0x4000
	s_nop 0
	global_load_lds_dwordx4 v14, s[64:65]
	s_add_u32 m0, s83, 0x5000
	s_nop 0
	global_load_lds_dwordx4 v20, s[66:67]
	s_add_u32 m0, s83, 0x6000
	s_nop 0
	global_load_lds_dwordx4 v21, s[66:67]
	s_add_u32 m0, s83, 0x7000
	s_nop 0
	global_load_lds_dwordx4 v22, s[66:67]
	s_add_u32 m0, s83, 0x8000
	s_nop 0
	global_load_lds_dwordx4 v23, s[66:67]
	s_add_u32 m0, s83, 0x9000
	s_nop 0
	global_load_lds_dwordx4 v24, s[66:67]
	s_add_u32 m0, s83, 0xa000
	s_nop 0
	global_load_lds_dwordx4 v25, s[66:67]
	s_add_u32 m0, s83, 0xb000
	s_nop 0
	global_load_lds_dwordx4 v26, s[66:67]
	s_add_u32 m0, s83, 0xc000
	s_nop 0
	global_load_lds_dwordx4 v27, s[66:67]
	s_add_u32 s64, s64, 0x80
	s_addc_u32 s65, s65, 0
	s_add_u32 s66, s66, 0x20000
	s_addc_u32 s67, s67, 0
	s_add_u32 s83, s70, s82
	s_add_u32 m0, s83, 0x0
	s_nop 0
	global_load_lds_dwordx4 v10, s[64:65]
	s_add_u32 m0, s83, 0x1000
	s_nop 0
	global_load_lds_dwordx4 v11, s[64:65]
	s_add_u32 m0, s83, 0x2000
	s_nop 0
	global_load_lds_dwordx4 v12, s[64:65]
	s_add_u32 m0, s83, 0x3000
	s_nop 0
	global_load_lds_dwordx4 v13, s[64:65]
	s_add_u32 m0, s83, 0x4000
	s_nop 0
	global_load_lds_dwordx4 v14, s[64:65]
	s_add_u32 m0, s83, 0x5000
	s_nop 0
	global_load_lds_dwordx4 v20, s[66:67]
	s_add_u32 m0, s83, 0x6000
	s_nop 0
	global_load_lds_dwordx4 v21, s[66:67]
	v_add_u32_e32 v34, s80, v30
	v_add_u32_e32 v35, s80, v31
	v_add_u32_e32 v36, s80, v32
	v_add_u32_e32 v37, s80, v33
	v_add_u32_e32 v48, s80, v40
	v_add_u32_e32 v49, s80, v41
	v_add_u32_e32 v50, s80, v42
	v_add_u32_e32 v51, s80, v43
	v_add_u32_e32 v52, s80, v44
	v_add_u32_e32 v53, s80, v45
	v_add_u32_e32 v54, s80, v46
	v_add_u32_e32 v55, s80, v47
	s_waitcnt vmcnt(20)
	s_barrier
	ds_read_b128 v[64:67], v34 offset:0
	ds_read_b128 v[68:71], v35 offset:2048
	ds_read_b128 v[72:75], v34 offset:4096
	ds_read_b128 v[76:79], v35 offset:6144
	ds_read_b128 v[80:83], v34 offset:8192
	ds_read_b64_tr_b16 v[100:101], v48 offset:0
	ds_read_b64_tr_b16 v[102:103], v48 offset:1024
	ds_read_b64_tr_b16 v[104:105], v49 offset:0
	ds_read_b64_tr_b16 v[106:107], v49 offset:1024
	ds_read_b64_tr_b16 v[108:109], v50 offset:0
	ds_read_b64_tr_b16 v[110:111], v50 offset:1024
	ds_read_b64_tr_b16 v[112:113], v51 offset:0
	ds_read_b64_tr_b16 v[114:115], v51 offset:1024
	ds_read_b64_tr_b16 v[116:117], v52 offset:0
	ds_read_b64_tr_b16 v[118:119], v52 offset:1024
	ds_read_b64_tr_b16 v[120:121], v53 offset:0
	ds_read_b64_tr_b16 v[122:123], v53 offset:1024
	ds_read_b64_tr_b16 v[124:125], v54 offset:0
	ds_read_b64_tr_b16 v[126:127], v54 offset:1024
	ds_read_b64_tr_b16 v[128:129], v55 offset:0
	ds_read_b64_tr_b16 v[130:131], v55 offset:1024
	s_mov_b32 s63, 29
.Lg2_loop:
	s_waitcnt lgkmcnt(0)
	s_add_u32 s83, s70, s82
	v_mfma_f32_16x16x32_f16 a[0:3], v[100:103], v[64:67], a[0:3]
	ds_read_b128 v[132:135], v36 offset:0
	v_mfma_f32_16x16x32_f16 a[32:35], v[100:103], v[68:71], a[32:35]
	ds_read_b128 v[136:139], v37 offset:2048
	s_add_u32 m0, s83, 0x7000
	v_mfma_f32_16x16x32_f16 a[64:67], v[100:103], v[72:75], a[64:67]
	global_load_lds_dwordx4 v22, s[66:67]
	ds_read_b128 v[140:143], v36 offset:4096
	v_mfma_f32_16x16x32_f16 a[96:99], v[100:103], v[76:79], a[96:99]
	ds_read_b128 v[144:147], v37 offset:6144
	v_mfma_f32_16x16x32_f16 a[128:131], v[100:103], v[80:83], a[128:131]
	ds_read_b128 v[148:151], v36 offset:8192
	v_mfma_f32_16x16x32_f16 a[4:7], v[104:107], v[64:67], a[4:7]
	ds_read_b64_tr_b16 v[168:169], v48 offset:8192
	v_mfma_f32_16x16x32_f16 a[36:39], v[104:107], v[68:71], a[36:39]
	ds_read_b64_tr_b16 v[170:171], v48 offset:9216
	v_mfma_f32_16x16x32_f16 a[68:71], v[104:107], v[72:75], a[68:71]
	ds_read_b64_tr_b16 v[172:173], v49 offset:8192
	s_add_u32 m0, s83, 0x8000
	v_mfma_f32_16x16x32_f16 a[100:103], v[104:107], v[76:79], a[100:103]
	global_load_lds_dwordx4 v23, s[66:67]
	ds_read_b64_tr_b16 v[174:175], v49 offset:9216
	v_mfma_f32_16x16x32_f16 a[132:135], v[104:107], v[80:83], a[132:135]
	ds_read_b64_tr_b16 v[176:177], v50 offset:8192
	v_mfma_f32_16x16x32_f16 a[8:11], v[108:111], v[64:67], a[8:11]
	ds_read_b64_tr_b16 v[178:179], v50 offset:9216
	v_mfma_f32_16x16x32_f16 a[40:43], v[108:111], v[68:71], a[40:43]
	ds_read_b64_tr_b16 v[180:181], v51 offset:8192
	v_mfma_f32_16x16x32_f16 a[72:75], v[108:111], v[72:75], a[72:75]
	ds_read_b64_tr_b16 v[182:183], v51 offset:9216
	v_mfma_f32_16x16x32_f16 a[104:107], v[108:111], v[76:79], a[104:107]
	ds_read_b64_tr_b16 v[184:185], v52 offset:8192
	s_add_u32 m0, s83, 0x9000
	v_mfma_f32_16x16x32_f16 a[136:139], v[108:111], v[80:83], a[136:139]
	global_load_lds_dwordx4 v24, s[66:67]
	ds_read_b64_tr_b16 v[186:187], v52 offset:9216
	v_mfma_f32_16x16x32_f16 a[12:15], v[112:115], v[64:67], a[12:15]
	ds_read_b64_tr_b16 v[188:189], v53 offset:8192
	v_mfma_f32_16x16x32_f16 a[44:47], v[112:115], v[68:71], a[44:47]
	ds_read_b64_tr_b16 v[190:191], v53 offset:9216
	v_mfma_f32_16x16x32_f16 a[76:79], v[112:115], v[72:75], a[76:79]
	ds_read_b64_tr_b16 v[192:193], v54 offset:8192
	v_mfma_f32_16x16x32_f16 a[108:111], v[112:115], v[76:79], a[108:111]
	ds_read_b64_tr_b16 v[194:195], v54 offset:9216
	v_mfma_f32_16x16x32_f16 a[140:143], v[112:115], v[80:83], a[140:143]
	ds_read_b64_tr_b16 v[196:197], v55 offset:8192
	s_add_u32 m0, s83, 0xa000
	v_mfma_f32_16x16x32_f16 a[16:19], v[116:119], v[64:67], a[16:19]
	global_load_lds_dwordx4 v25, s[66:67]
	ds_read_b64_tr_b16 v[198:199], v55 offset:9216
	v_mfma_f32_16x16x32_f16 a[48:51], v[116:119], v[68:71], a[48:51]
	v_add_u32_e32 v34, s81, v30
	v_mfma_f32_16x16x32_f16 a[80:83], v[116:119], v[72:75], a[80:83]
	v_add_u32_e32 v35, s81, v31
	v_mfma_f32_16x16x32_f16 a[112:115], v[116:119], v[76:79], a[112:115]
	v_add_u32_e32 v36, s81, v32
	v_mfma_f32_16x16x32_f16 a[144:147], v[116:119], v[80:83], a[144:147]
	v_add_u32_e32 v37, s81, v33
	v_mfma_f32_16x16x32_f16 a[20:23], v[120:123], v[64:67], a[20:23]
	v_add_u32_e32 v48, s81, v40
	s_add_u32 m0, s83, 0xb000
	v_mfma_f32_16x16x32_f16 a[52:55], v[120:123], v[68:71], a[52:55]
	global_load_lds_dwordx4 v26, s[66:67]
	v_add_u32_e32 v49, s81, v41
	v_mfma_f32_16x16x32_f16 a[84:87], v[120:123], v[72:75], a[84:87]
	v_add_u32_e32 v50, s81, v42
	v_mfma_f32_16x16x32_f16 a[116:119], v[120:123], v[76:79], a[116:119]
	v_add_u32_e32 v51, s81, v43
	v_mfma_f32_16x16x32_f16 a[148:151], v[120:123], v[80:83], a[148:151]
	v_add_u32_e32 v52, s81, v44
	v_mfma_f32_16x16x32_f16 a[24:27], v[124:127], v[64:67], a[24:27]
	v_add_u32_e32 v53, s81, v45
	v_mfma_f32_16x16x32_f16 a[56:59], v[124:127], v[68:71], a[56:59]
	v_add_u32_e32 v54, s81, v46
	s_add_u32 m0, s83, 0xc000
	v_mfma_f32_16x16x32_f16 a[88:91], v[124:127], v[72:75], a[88:91]
	global_load_lds_dwordx4 v27, s[66:67]
	v_add_u32_e32 v55, s81, v47
	v_mfma_f32_16x16x32_f16 a[120:123], v[124:127], v[76:79], a[120:123]
	v_mfma_f32_16x16x32_f16 a[152:155], v[124:127], v[80:83], a[152:155]
	v_mfma_f32_16x16x32_f16 a[28:31], v[128:131], v[64:67], a[28:31]
	v_mfma_f32_16x16x32_f16 a[60:63], v[128:131], v[68:71], a[60:63]
	v_mfma_f32_16x16x32_f16 a[92:95], v[128:131], v[72:75], a[92:95]
	v_mfma_f32_16x16x32_f16 a[124:127], v[128:131], v[76:79], a[124:127]
	v_mfma_f32_16x16x32_f16 a[156:159], v[128:131], v[80:83], a[156:159]
	s_add_u32 s64, s64, 0x80
	s_addc_u32 s65, s65, 0
	s_add_u32 s66, s66, 0x20000
	s_addc_u32 s67, s67, 0
	s_waitcnt vmcnt(13) lgkmcnt(0)
	s_barrier
	s_add_u32 s83, s70, s80
	v_mfma_f32_16x16x32_f16 a[0:3], v[168:171], v[132:135], a[0:3]
	ds_read_b128 v[64:67], v34 offset:0
	v_mfma_f32_16x16x32_f16 a[32:35], v[168:171], v[136:139], a[32:35]
	ds_read_b128 v[68:71], v35 offset:2048
	s_add_u32 m0, s83, 0x0
	v_mfma_f32_16x16x32_f16 a[64:67], v[168:171], v[140:143], a[64:67]
	global_load_lds_dwordx4 v10, s[64:65]
	ds_read_b128 v[72:75], v34 offset:4096
	v_mfma_f32_16x16x32_f16 a[96:99], v[168:171], v[144:147], a[96:99]
	ds_read_b128 v[76:79], v35 offset:6144
	v_mfma_f32_16x16x32_f16 a[128:131], v[168:171], v[148:151], a[128:131]
	ds_read_b128 v[80:83], v34 offset:8192
	v_mfma_f32_16x16x32_f16 a[4:7], v[172:175], v[132:135], a[4:7]
	ds_read_b64_tr_b16 v[100:101], v48 offset:0
	v_mfma_f32_16x16x32_f16 a[36:39], v[172:175], v[136:139], a[36:39]
	ds_read_b64_tr_b16 v[102:103], v48 offset:1024
	s_add_u32 m0, s83, 0x1000
	v_mfma_f32_16x16x32_f16 a[68:71], v[172:175], v[140:143], a[68:71]
	global_load_lds_dwordx4 v11, s[64:65]
	ds_read_b64_tr_b16 v[104:105], v49 offset:0
	v_mfma_f32_16x16x32_f16 a[100:103], v[172:175], v[144:147], a[100:103]
	ds_read_b64_tr_b16 v[106:107], v49 offset:1024
	v_mfma_f32_16x16x32_f16 a[132:135], v[172:175], v[148:151], a[132:135]
	ds_read_b64_tr_b16 v[108:109], v50 offset:0
	v_mfma_f32_16x16x32_f16 a[8:11], v[176:179], v[132:135], a[8:11]
	ds_read_b64_tr_b16 v[110:111], v50 offset:1024
	v_mfma_f32_16x16x32_f16 a[40:43], v[176:179], v[136:139], a[40:43]
	ds_read_b64_tr_b16 v[112:113], v51 offset:0
	s_add_u32 m0, s83, 0x2000
	v_mfma_f32_16x16x32_f16 a[72:75], v[176:179], v[140:143], a[72:75]
	global_load_lds_dwordx4 v12, s[64:65]
	ds_read_b64_tr_b16 v[114:115], v51 offset:1024
	v_mfma_f32_16x16x32_f16 a[104:107], v[176:179], v[144:147], a[104:107]
	ds_read_b64_tr_b16 v[116:117], v52 offset:0
	v_mfma_f32_16x16x32_f16 a[136:139], v[176:179], v[148:151], a[136:139]
	ds_read_b64_tr_b16 v[118:119], v52 offset:1024
	v_mfma_f32_16x16x32_f16 a[12:15], v[180:183], v[132:135], a[12:15]
	ds_read_b64_tr_b16 v[120:121], v53 offset:0
	v_mfma_f32_16x16x32_f16 a[44:47], v[180:183], v[136:139], a[44:47]
	ds_read_b64_tr_b16 v[122:123], v53 offset:1024
	s_add_u32 m0, s83, 0x3000
	v_mfma_f32_16x16x32_f16 a[76:79], v[180:183], v[140:143], a[76:79]
	global_load_lds_dwordx4 v13, s[64:65]
	ds_read_b64_tr_b16 v[124:125], v54 offset:0
	v_mfma_f32_16x16x32_f16 a[108:111], v[180:183], v[144:147], a[108:111]
	ds_read_b64_tr_b16 v[126:127], v54 offset:1024
	v_mfma_f32_16x16x32_f16 a[140:143], v[180:183], v[148:151], a[140:143]
	ds_read_b64_tr_b16 v[128:129], v55 offset:0
	v_mfma_f32_16x16x32_f16 a[16:19], v[184:187], v[132:135], a[16:19]
	ds_read_b64_tr_b16 v[130:131], v55 offset:1024
	v_mfma_f32_16x16x32_f16 a[48:51], v[184:187], v[136:139], a[48:51]
	s_add_u32 m0, s83, 0x4000
	v_mfma_f32_16x16x32_f16 a[80:83], v[184:187], v[140:143], a[80:83]
	global_load_lds_dwordx4 v14, s[64:65]
	v_mfma_f32_16x16x32_f16 a[112:115], v[184:187], v[144:147], a[112:115]
	v_mfma_f32_16x16x32_f16 a[144:147], v[184:187], v[148:151], a[144:147]
	v_mfma_f32_16x16x32_f16 a[20:23], v[188:191], v[132:135], a[20:23]
	v_mfma_f32_16x16x32_f16 a[52:55], v[188:191], v[136:139], a[52:55]
	s_add_u32 m0, s83, 0x5000
	v_mfma_f32_16x16x32_f16 a[84:87], v[188:191], v[140:143], a[84:87]
	global_load_lds_dwordx4 v20, s[66:67]
	v_mfma_f32_16x16x32_f16 a[116:119], v[188:191], v[144:147], a[116:119]
	v_mfma_f32_16x16x32_f16 a[148:151], v[188:191], v[148:151], a[148:151]
	v_mfma_f32_16x16x32_f16 a[24:27], v[192:195], v[132:135], a[24:27]
	v_mfma_f32_16x16x32_f16 a[56:59], v[192:195], v[136:139], a[56:59]
	s_add_u32 m0, s83, 0x6000
	v_mfma_f32_16x16x32_f16 a[88:91], v[192:195], v[140:143], a[88:91]
	global_load_lds_dwordx4 v21, s[66:67]
	v_mfma_f32_16x16x32_f16 a[120:123], v[192:195], v[144:147], a[120:123]
	v_mfma_f32_16x16x32_f16 a[152:155], v[192:195], v[148:151], a[152:155]
	v_mfma_f32_16x16x32_f16 a[28:31], v[196:199], v[132:135], a[28:31]
	v_mfma_f32_16x16x32_f16 a[60:63], v[196:199], v[136:139], a[60:63]
	v_mfma_f32_16x16x32_f16 a[92:95], v[196:199], v[140:143], a[92:95]
	v_mfma_f32_16x16x32_f16 a[124:127], v[196:199], v[144:147], a[124:127]
	v_mfma_f32_16x16x32_f16 a[156:159], v[196:199], v[148:151], a[156:159]
	s_mov_b32 s22, s80
	s_mov_b32 s80, s81
	s_mov_b32 s81, s82
	s_mov_b32 s82, s22
	s_sub_u32 s63, s63, 1
	s_cmp_lg_u32 s63, 0
	s_cbranch_scc1 .Lg2_loop
	s_waitcnt lgkmcnt(0)
	s_add_u32 s83, s70, s82
	v_mfma_f32_16x16x32_f16 a[0:3], v[100:103], v[64:67], a[0:3]
	ds_read_b128 v[132:135], v36 offset:0
	v_mfma_f32_16x16x32_f16 a[32:35], v[100:103], v[68:71], a[32:35]
	ds_read_b128 v[136:139], v37 offset:2048
	s_add_u32 m0, s83, 0x7000
	v_mfma_f32_16x16x32_f16 a[64:67], v[100:103], v[72:75], a[64:67]
	global_load_lds_dwordx4 v22, s[66:67]
	ds_read_b128 v[140:143], v36 offset:4096
	v_mfma_f32_16x16x32_f16 a[96:99], v[100:103], v[76:79], a[96:99]
	ds_read_b128 v[144:147], v37 offset:6144
	v_mfma_f32_16x16x32_f16 a[128:131], v[100:103], v[80:83], a[128:131]
	ds_read_b128 v[148:151], v36 offset:8192
	v_mfma_f32_16x16x32_f16 a[4:7], v[104:107], v[64:67], a[4:7]
	ds_read_b64_tr_b16 v[168:169], v48 offset:8192
	v_mfma_f32_16x16x32_f16 a[36:39], v[104:107], v[68:71], a[36:39]
	ds_read_b64_tr_b16 v[170:171], v48 offset:9216
	v_mfma_f32_16x16x32_f16 a[68:71], v[104:107], v[72:75], a[68:71]
	ds_read_b64_tr_b16 v[172:173], v49 offset:8192
	s_add_u32 m0, s83, 0x8000
	v_mfma_f32_16x16x32_f16 a[100:103], v[104:107], v[76:79], a[100:103]
	global_load_lds_dwordx4 v23, s[66:67]
	ds_read_b64_tr_b16 v[174:175], v49 offset:9216
	v_mfma_f32_16x16x32_f16 a[132:135], v[104:107], v[80:83], a[132:135]
	ds_read_b64_tr_b16 v[176:177], v50 offset:8192
	v_mfma_f32_16x16x32_f16 a[8:11], v[108:111], v[64:67], a[8:11]
	ds_read_b64_tr_b16 v[178:179], v50 offset:9216
	v_mfma_f32_16x16x32_f16 a[40:43], v[108:111], v[68:71], a[40:43]
	ds_read_b64_tr_b16 v[180:181], v51 offset:8192
	v_mfma_f32_16x16x32_f16 a[72:75], v[108:111], v[72:75], a[72:75]
	ds_read_b64_tr_b16 v[182:183], v51 offset:9216
	v_mfma_f32_16x16x32_f16 a[104:107], v[108:111], v[76:79], a[104:107]
	ds_read_b64_tr_b16 v[184:185], v52 offset:8192
	s_add_u32 m0, s83, 0x9000
	v_mfma_f32_16x16x32_f16 a[136:139], v[108:111], v[80:83], a[136:139]
	global_load_lds_dwordx4 v24, s[66:67]
	ds_read_b64_tr_b16 v[186:187], v52 offset:9216
	v_mfma_f32_16x16x32_f16 a[12:15], v[112:115], v[64:67], a[12:15]
	ds_read_b64_tr_b16 v[188:189], v53 offset:8192
	v_mfma_f32_16x16x32_f16 a[44:47], v[112:115], v[68:71], a[44:47]
	ds_read_b64_tr_b16 v[190:191], v53 offset:9216
	v_mfma_f32_16x16x32_f16 a[76:79], v[112:115], v[72:75], a[76:79]
	ds_read_b64_tr_b16 v[192:193], v54 offset:8192
	v_mfma_f32_16x16x32_f16 a[108:111], v[112:115], v[76:79], a[108:111]
	ds_read_b64_tr_b16 v[194:195], v54 offset:9216
	v_mfma_f32_16x16x32_f16 a[140:143], v[112:115], v[80:83], a[140:143]
	ds_read_b64_tr_b16 v[196:197], v55 offset:8192
	s_add_u32 m0, s83, 0xa000
	v_mfma_f32_16x16x32_f16 a[16:19], v[116:119], v[64:67], a[16:19]
	global_load_lds_dwordx4 v25, s[66:67]
	ds_read_b64_tr_b16 v[198:199], v55 offset:9216
	v_mfma_f32_16x16x32_f16 a[48:51], v[116:119], v[68:71], a[48:51]
	v_add_u32_e32 v34, s81, v30
	v_mfma_f32_16x16x32_f16 a[80:83], v[116:119], v[72:75], a[80:83]
	v_add_u32_e32 v35, s81, v31
	v_mfma_f32_16x16x32_f16 a[112:115], v[116:119], v[76:79], a[112:115]
	v_add_u32_e32 v36, s81, v32
	v_mfma_f32_16x16x32_f16 a[144:147], v[116:119], v[80:83], a[144:147]
	v_add_u32_e32 v37, s81, v33
	v_mfma_f32_16x16x32_f16 a[20:23], v[120:123], v[64:67], a[20:23]
	v_add_u32_e32 v48, s81, v40
	s_add_u32 m0, s83, 0xb000
	v_mfma_f32_16x16x32_f16 a[52:55], v[120:123], v[68:71], a[52:55]
	global_load_lds_dwordx4 v26, s[66:67]
	v_add_u32_e32 v49, s81, v41
	v_mfma_f32_16x16x32_f16 a[84:87], v[120:123], v[72:75], a[84:87]
	v_add_u32_e32 v50, s81, v42
	v_mfma_f32_16x16x32_f16 a[116:119], v[120:123], v[76:79], a[116:119]
	v_add_u32_e32 v51, s81, v43
	v_mfma_f32_16x16x32_f16 a[148:151], v[120:123], v[80:83], a[148:151]
	v_add_u32_e32 v52, s81, v44
	v_mfma_f32_16x16x32_f16 a[24:27], v[124:127], v[64:67], a[24:27]
	v_add_u32_e32 v53, s81, v45
	v_mfma_f32_16x16x32_f16 a[56:59], v[124:127], v[68:71], a[56:59]
	v_add_u32_e32 v54, s81, v46
	s_add_u32 m0, s83, 0xc000
	v_mfma_f32_16x16x32_f16 a[88:91], v[124:127], v[72:75], a[88:91]
	global_load_lds_dwordx4 v27, s[66:67]
	v_add_u32_e32 v55, s81, v47
	v_mfma_f32_16x16x32_f16 a[120:123], v[124:127], v[76:79], a[120:123]
	v_mfma_f32_16x16x32_f16 a[152:155], v[124:127], v[80:83], a[152:155]
	v_mfma_f32_16x16x32_f16 a[28:31], v[128:131], v[64:67], a[28:31]
	v_mfma_f32_16x16x32_f16 a[60:63], v[128:131], v[68:71], a[60:63]
	v_mfma_f32_16x16x32_f16 a[92:95], v[128:131], v[72:75], a[92:95]
	v_mfma_f32_16x16x32_f16 a[124:127], v[128:131], v[76:79], a[124:127]
	v_mfma_f32_16x16x32_f16 a[156:159], v[128:131], v[80:83], a[156:159]
	s_add_u32 s64, s64, 0x80
	s_addc_u32 s65, s65, 0
	s_add_u32 s66, s66, 0x20000
	s_addc_u32 s67, s67, 0
	s_waitcnt vmcnt(13) lgkmcnt(0)
	s_barrier
	v_mfma_f32_16x16x32_f16 a[0:3], v[168:171], v[132:135], a[0:3]
	ds_read_b128 v[64:67], v34 offset:0
	v_mfma_f32_16x16x32_f16 a[32:35], v[168:171], v[136:139], a[32:35]
	ds_read_b128 v[68:71], v35 offset:2048
	v_mfma_f32_16x16x32_f16 a[64:67], v[168:171], v[140:143], a[64:67]
	ds_read_b128 v[72:75], v34 offset:4096
	v_mfma_f32_16x16x32_f16 a[96:99], v[168:171], v[144:147], a[96:99]
	ds_read_b128 v[76:79], v35 offset:6144
	v_mfma_f32_16x16x32_f16 a[128:131], v[168:171], v[148:151], a[128:131]
	ds_read_b128 v[80:83], v34 offset:8192
	v_mfma_f32_16x16x32_f16 a[4:7], v[172:175], v[132:135], a[4:7]
	ds_read_b64_tr_b16 v[100:101], v48 offset:0
	v_mfma_f32_16x16x32_f16 a[36:39], v[172:175], v[136:139], a[36:39]
	ds_read_b64_tr_b16 v[102:103], v48 offset:1024
	v_mfma_f32_16x16x32_f16 a[68:71], v[172:175], v[140:143], a[68:71]
	ds_read_b64_tr_b16 v[104:105], v49 offset:0
	v_mfma_f32_16x16x32_f16 a[100:103], v[172:175], v[144:147], a[100:103]
	ds_read_b64_tr_b16 v[106:107], v49 offset:1024
	v_mfma_f32_16x16x32_f16 a[132:135], v[172:175], v[148:151], a[132:135]
	ds_read_b64_tr_b16 v[108:109], v50 offset:0
	v_mfma_f32_16x16x32_f16 a[8:11], v[176:179], v[132:135], a[8:11]
	ds_read_b64_tr_b16 v[110:111], v50 offset:1024
	v_mfma_f32_16x16x32_f16 a[40:43], v[176:179], v[136:139], a[40:43]
	ds_read_b64_tr_b16 v[112:113], v51 offset:0
	v_mfma_f32_16x16x32_f16 a[72:75], v[176:179], v[140:143], a[72:75]
	ds_read_b64_tr_b16 v[114:115], v51 offset:1024
	v_mfma_f32_16x16x32_f16 a[104:107], v[176:179], v[144:147], a[104:107]
	ds_read_b64_tr_b16 v[116:117], v52 offset:0
	v_mfma_f32_16x16x32_f16 a[136:139], v[176:179], v[148:151], a[136:139]
	ds_read_b64_tr_b16 v[118:119], v52 offset:1024
	v_mfma_f32_16x16x32_f16 a[12:15], v[180:183], v[132:135], a[12:15]
	ds_read_b64_tr_b16 v[120:121], v53 offset:0
	v_mfma_f32_16x16x32_f16 a[44:47], v[180:183], v[136:139], a[44:47]
	ds_read_b64_tr_b16 v[122:123], v53 offset:1024
	v_mfma_f32_16x16x32_f16 a[76:79], v[180:183], v[140:143], a[76:79]
	ds_read_b64_tr_b16 v[124:125], v54 offset:0
	v_mfma_f32_16x16x32_f16 a[108:111], v[180:183], v[144:147], a[108:111]
	ds_read_b64_tr_b16 v[126:127], v54 offset:1024
	v_mfma_f32_16x16x32_f16 a[140:143], v[180:183], v[148:151], a[140:143]
	ds_read_b64_tr_b16 v[128:129], v55 offset:0
	v_mfma_f32_16x16x32_f16 a[16:19], v[184:187], v[132:135], a[16:19]
	ds_read_b64_tr_b16 v[130:131], v55 offset:1024
	v_mfma_f32_16x16x32_f16 a[48:51], v[184:187], v[136:139], a[48:51]
	v_mfma_f32_16x16x32_f16 a[80:83], v[184:187], v[140:143], a[80:83]
	v_mfma_f32_16x16x32_f16 a[112:115], v[184:187], v[144:147], a[112:115]
	v_mfma_f32_16x16x32_f16 a[144:147], v[184:187], v[148:151], a[144:147]
	v_mfma_f32_16x16x32_f16 a[20:23], v[188:191], v[132:135], a[20:23]
	v_mfma_f32_16x16x32_f16 a[52:55], v[188:191], v[136:139], a[52:55]
	v_mfma_f32_16x16x32_f16 a[84:87], v[188:191], v[140:143], a[84:87]
	v_mfma_f32_16x16x32_f16 a[116:119], v[188:191], v[144:147], a[116:119]
	v_mfma_f32_16x16x32_f16 a[148:151], v[188:191], v[148:151], a[148:151]
	v_mfma_f32_16x16x32_f16 a[24:27], v[192:195], v[132:135], a[24:27]
	v_mfma_f32_16x16x32_f16 a[56:59], v[192:195], v[136:139], a[56:59]
	v_mfma_f32_16x16x32_f16 a[88:91], v[192:195], v[140:143], a[88:91]
	v_mfma_f32_16x16x32_f16 a[120:123], v[192:195], v[144:147], a[120:123]
	v_mfma_f32_16x16x32_f16 a[152:155], v[192:195], v[148:151], a[152:155]
	v_mfma_f32_16x16x32_f16 a[28:31], v[196:199], v[132:135], a[28:31]
	v_mfma_f32_16x16x32_f16 a[60:63], v[196:199], v[136:139], a[60:63]
	v_mfma_f32_16x16x32_f16 a[92:95], v[196:199], v[140:143], a[92:95]
	v_mfma_f32_16x16x32_f16 a[124:127], v[196:199], v[144:147], a[124:127]
	v_mfma_f32_16x16x32_f16 a[156:159], v[196:199], v[148:151], a[156:159]
	s_mov_b32 s22, s80
	s_mov_b32 s80, s81
	s_mov_b32 s81, s82
	s_mov_b32 s82, s22
	s_waitcnt lgkmcnt(0)
	v_mfma_f32_16x16x32_f16 a[0:3], v[100:103], v[64:67], a[0:3]
	ds_read_b128 v[132:135], v36 offset:0
	v_mfma_f32_16x16x32_f16 a[32:35], v[100:103], v[68:71], a[32:35]
	ds_read_b128 v[136:139], v37 offset:2048
	v_mfma_f32_16x16x32_f16 a[64:67], v[100:103], v[72:75], a[64:67]
	ds_read_b128 v[140:143], v36 offset:4096
	v_mfma_f32_16x16x32_f16 a[96:99], v[100:103], v[76:79], a[96:99]
	ds_read_b128 v[144:147], v37 offset:6144
	v_mfma_f32_16x16x32_f16 a[128:131], v[100:103], v[80:83], a[128:131]
	ds_read_b128 v[148:151], v36 offset:8192
	v_mfma_f32_16x16x32_f16 a[4:7], v[104:107], v[64:67], a[4:7]
	ds_read_b64_tr_b16 v[168:169], v48 offset:8192
	v_mfma_f32_16x16x32_f16 a[36:39], v[104:107], v[68:71], a[36:39]
	ds_read_b64_tr_b16 v[170:171], v48 offset:9216
	v_mfma_f32_16x16x32_f16 a[68:71], v[104:107], v[72:75], a[68:71]
	ds_read_b64_tr_b16 v[172:173], v49 offset:8192
	v_mfma_f32_16x16x32_f16 a[100:103], v[104:107], v[76:79], a[100:103]
	ds_read_b64_tr_b16 v[174:175], v49 offset:9216
	v_mfma_f32_16x16x32_f16 a[132:135], v[104:107], v[80:83], a[132:135]
	ds_read_b64_tr_b16 v[176:177], v50 offset:8192
	v_mfma_f32_16x16x32_f16 a[8:11], v[108:111], v[64:67], a[8:11]
	ds_read_b64_tr_b16 v[178:179], v50 offset:9216
	v_mfma_f32_16x16x32_f16 a[40:43], v[108:111], v[68:71], a[40:43]
	ds_read_b64_tr_b16 v[180:181], v51 offset:8192
	v_mfma_f32_16x16x32_f16 a[72:75], v[108:111], v[72:75], a[72:75]
	ds_read_b64_tr_b16 v[182:183], v51 offset:9216
	v_mfma_f32_16x16x32_f16 a[104:107], v[108:111], v[76:79], a[104:107]
	ds_read_b64_tr_b16 v[184:185], v52 offset:8192
	v_mfma_f32_16x16x32_f16 a[136:139], v[108:111], v[80:83], a[136:139]
	ds_read_b64_tr_b16 v[186:187], v52 offset:9216
	v_mfma_f32_16x16x32_f16 a[12:15], v[112:115], v[64:67], a[12:15]
	ds_read_b64_tr_b16 v[188:189], v53 offset:8192
	v_mfma_f32_16x16x32_f16 a[44:47], v[112:115], v[68:71], a[44:47]
	ds_read_b64_tr_b16 v[190:191], v53 offset:9216
	v_mfma_f32_16x16x32_f16 a[76:79], v[112:115], v[72:75], a[76:79]
	ds_read_b64_tr_b16 v[192:193], v54 offset:8192
	v_mfma_f32_16x16x32_f16 a[108:111], v[112:115], v[76:79], a[108:111]
	ds_read_b64_tr_b16 v[194:195], v54 offset:9216
	v_mfma_f32_16x16x32_f16 a[140:143], v[112:115], v[80:83], a[140:143]
	ds_read_b64_tr_b16 v[196:197], v55 offset:8192
	v_mfma_f32_16x16x32_f16 a[16:19], v[116:119], v[64:67], a[16:19]
	ds_read_b64_tr_b16 v[198:199], v55 offset:9216
	v_mfma_f32_16x16x32_f16 a[48:51], v[116:119], v[68:71], a[48:51]
	v_add_u32_e32 v34, s81, v30
	v_mfma_f32_16x16x32_f16 a[80:83], v[116:119], v[72:75], a[80:83]
	v_add_u32_e32 v35, s81, v31
	v_mfma_f32_16x16x32_f16 a[112:115], v[116:119], v[76:79], a[112:115]
	v_add_u32_e32 v36, s81, v32
	v_mfma_f32_16x16x32_f16 a[144:147], v[116:119], v[80:83], a[144:147]
	v_add_u32_e32 v37, s81, v33
	v_mfma_f32_16x16x32_f16 a[20:23], v[120:123], v[64:67], a[20:23]
	v_add_u32_e32 v48, s81, v40
	v_mfma_f32_16x16x32_f16 a[52:55], v[120:123], v[68:71], a[52:55]
	v_add_u32_e32 v49, s81, v41
	v_mfma_f32_16x16x32_f16 a[84:87], v[120:123], v[72:75], a[84:87]
	v_add_u32_e32 v50, s81, v42
	v_mfma_f32_16x16x32_f16 a[116:119], v[120:123], v[76:79], a[116:119]
	v_add_u32_e32 v51, s81, v43
	v_mfma_f32_16x16x32_f16 a[148:151], v[120:123], v[80:83], a[148:151]
	v_add_u32_e32 v52, s81, v44
	v_mfma_f32_16x16x32_f16 a[24:27], v[124:127], v[64:67], a[24:27]
	v_add_u32_e32 v53, s81, v45
	v_mfma_f32_16x16x32_f16 a[56:59], v[124:127], v[68:71], a[56:59]
	v_add_u32_e32 v54, s81, v46
	v_mfma_f32_16x16x32_f16 a[88:91], v[124:127], v[72:75], a[88:91]
	v_add_u32_e32 v55, s81, v47
	v_mfma_f32_16x16x32_f16 a[120:123], v[124:127], v[76:79], a[120:123]
	v_mfma_f32_16x16x32_f16 a[152:155], v[124:127], v[80:83], a[152:155]
	v_mfma_f32_16x16x32_f16 a[28:31], v[128:131], v[64:67], a[28:31]
	v_mfma_f32_16x16x32_f16 a[60:63], v[128:131], v[68:71], a[60:63]
	v_mfma_f32_16x16x32_f16 a[92:95], v[128:131], v[72:75], a[92:95]
	v_mfma_f32_16x16x32_f16 a[124:127], v[128:131], v[76:79], a[124:127]
	v_mfma_f32_16x16x32_f16 a[156:159], v[128:131], v[80:83], a[156:159]
	s_waitcnt vmcnt(0) lgkmcnt(0)
	s_barrier
	v_mfma_f32_16x16x32_f16 a[0:3], v[168:171], v[132:135], a[0:3]
	ds_read_b128 v[64:67], v34 offset:0
	v_mfma_f32_16x16x32_f16 a[32:35], v[168:171], v[136:139], a[32:35]
	ds_read_b128 v[68:71], v35 offset:2048
	v_mfma_f32_16x16x32_f16 a[64:67], v[168:171], v[140:143], a[64:67]
	ds_read_b128 v[72:75], v34 offset:4096
	v_mfma_f32_16x16x32_f16 a[96:99], v[168:171], v[144:147], a[96:99]
	ds_read_b128 v[76:79], v35 offset:6144
	v_mfma_f32_16x16x32_f16 a[128:131], v[168:171], v[148:151], a[128:131]
	ds_read_b128 v[80:83], v34 offset:8192
	v_mfma_f32_16x16x32_f16 a[4:7], v[172:175], v[132:135], a[4:7]
	ds_read_b64_tr_b16 v[100:101], v48 offset:0
	v_mfma_f32_16x16x32_f16 a[36:39], v[172:175], v[136:139], a[36:39]
	ds_read_b64_tr_b16 v[102:103], v48 offset:1024
	v_mfma_f32_16x16x32_f16 a[68:71], v[172:175], v[140:143], a[68:71]
	ds_read_b64_tr_b16 v[104:105], v49 offset:0
	v_mfma_f32_16x16x32_f16 a[100:103], v[172:175], v[144:147], a[100:103]
	ds_read_b64_tr_b16 v[106:107], v49 offset:1024
	v_mfma_f32_16x16x32_f16 a[132:135], v[172:175], v[148:151], a[132:135]
	ds_read_b64_tr_b16 v[108:109], v50 offset:0
	v_mfma_f32_16x16x32_f16 a[8:11], v[176:179], v[132:135], a[8:11]
	ds_read_b64_tr_b16 v[110:111], v50 offset:1024
	v_mfma_f32_16x16x32_f16 a[40:43], v[176:179], v[136:139], a[40:43]
	ds_read_b64_tr_b16 v[112:113], v51 offset:0
	v_mfma_f32_16x16x32_f16 a[72:75], v[176:179], v[140:143], a[72:75]
	ds_read_b64_tr_b16 v[114:115], v51 offset:1024
	v_mfma_f32_16x16x32_f16 a[104:107], v[176:179], v[144:147], a[104:107]
	ds_read_b64_tr_b16 v[116:117], v52 offset:0
	v_mfma_f32_16x16x32_f16 a[136:139], v[176:179], v[148:151], a[136:139]
	ds_read_b64_tr_b16 v[118:119], v52 offset:1024
	v_mfma_f32_16x16x32_f16 a[12:15], v[180:183], v[132:135], a[12:15]
	ds_read_b64_tr_b16 v[120:121], v53 offset:0
	v_mfma_f32_16x16x32_f16 a[44:47], v[180:183], v[136:139], a[44:47]
	ds_read_b64_tr_b16 v[122:123], v53 offset:1024
	v_mfma_f32_16x16x32_f16 a[76:79], v[180:183], v[140:143], a[76:79]
	ds_read_b64_tr_b16 v[124:125], v54 offset:0
	v_mfma_f32_16x16x32_f16 a[108:111], v[180:183], v[144:147], a[108:111]
	ds_read_b64_tr_b16 v[126:127], v54 offset:1024
	v_mfma_f32_16x16x32_f16 a[140:143], v[180:183], v[148:151], a[140:143]
	ds_read_b64_tr_b16 v[128:129], v55 offset:0
	v_mfma_f32_16x16x32_f16 a[16:19], v[184:187], v[132:135], a[16:19]
	ds_read_b64_tr_b16 v[130:131], v55 offset:1024
	v_mfma_f32_16x16x32_f16 a[48:51], v[184:187], v[136:139], a[48:51]
	v_mfma_f32_16x16x32_f16 a[80:83], v[184:187], v[140:143], a[80:83]
	v_mfma_f32_16x16x32_f16 a[112:115], v[184:187], v[144:147], a[112:115]
	v_mfma_f32_16x16x32_f16 a[144:147], v[184:187], v[148:151], a[144:147]
	v_mfma_f32_16x16x32_f16 a[20:23], v[188:191], v[132:135], a[20:23]
	v_mfma_f32_16x16x32_f16 a[52:55], v[188:191], v[136:139], a[52:55]
	v_mfma_f32_16x16x32_f16 a[84:87], v[188:191], v[140:143], a[84:87]
	v_mfma_f32_16x16x32_f16 a[116:119], v[188:191], v[144:147], a[116:119]
	v_mfma_f32_16x16x32_f16 a[148:151], v[188:191], v[148:151], a[148:151]
	v_mfma_f32_16x16x32_f16 a[24:27], v[192:195], v[132:135], a[24:27]
	v_mfma_f32_16x16x32_f16 a[56:59], v[192:195], v[136:139], a[56:59]
	v_mfma_f32_16x16x32_f16 a[88:91], v[192:195], v[140:143], a[88:91]
	v_mfma_f32_16x16x32_f16 a[120:123], v[192:195], v[144:147], a[120:123]
	v_mfma_f32_16x16x32_f16 a[152:155], v[192:195], v[148:151], a[152:155]
	v_mfma_f32_16x16x32_f16 a[28:31], v[196:199], v[132:135], a[28:31]
	v_mfma_f32_16x16x32_f16 a[60:63], v[196:199], v[136:139], a[60:63]
	v_mfma_f32_16x16x32_f16 a[92:95], v[196:199], v[140:143], a[92:95]
	v_mfma_f32_16x16x32_f16 a[124:127], v[196:199], v[144:147], a[124:127]
	v_mfma_f32_16x16x32_f16 a[156:159], v[196:199], v[148:151], a[156:159]
	s_mov_b32 s22, s80
	s_mov_b32 s80, s81
	s_mov_b32 s81, s82
	s_mov_b32 s82, s22
	s_waitcnt lgkmcnt(0)
	v_mfma_f32_16x16x32_f16 a[0:3], v[100:103], v[64:67], a[0:3]
	ds_read_b128 v[132:135], v36 offset:0
	v_mfma_f32_16x16x32_f16 a[32:35], v[100:103], v[68:71], a[32:35]
	ds_read_b128 v[136:139], v37 offset:2048
	v_mfma_f32_16x16x32_f16 a[64:67], v[100:103], v[72:75], a[64:67]
	ds_read_b128 v[140:143], v36 offset:4096
	v_mfma_f32_16x16x32_f16 a[96:99], v[100:103], v[76:79], a[96:99]
	ds_read_b128 v[144:147], v37 offset:6144
	v_mfma_f32_16x16x32_f16 a[128:131], v[100:103], v[80:83], a[128:131]
	ds_read_b128 v[148:151], v36 offset:8192
	v_mfma_f32_16x16x32_f16 a[4:7], v[104:107], v[64:67], a[4:7]
	ds_read_b64_tr_b16 v[168:169], v48 offset:8192
	v_mfma_f32_16x16x32_f16 a[36:39], v[104:107], v[68:71], a[36:39]
	ds_read_b64_tr_b16 v[170:171], v48 offset:9216
	v_mfma_f32_16x16x32_f16 a[68:71], v[104:107], v[72:75], a[68:71]
	ds_read_b64_tr_b16 v[172:173], v49 offset:8192
	v_mfma_f32_16x16x32_f16 a[100:103], v[104:107], v[76:79], a[100:103]
	ds_read_b64_tr_b16 v[174:175], v49 offset:9216
	v_mfma_f32_16x16x32_f16 a[132:135], v[104:107], v[80:83], a[132:135]
	ds_read_b64_tr_b16 v[176:177], v50 offset:8192
	v_mfma_f32_16x16x32_f16 a[8:11], v[108:111], v[64:67], a[8:11]
	ds_read_b64_tr_b16 v[178:179], v50 offset:9216
	v_mfma_f32_16x16x32_f16 a[40:43], v[108:111], v[68:71], a[40:43]
	ds_read_b64_tr_b16 v[180:181], v51 offset:8192
	v_mfma_f32_16x16x32_f16 a[72:75], v[108:111], v[72:75], a[72:75]
	ds_read_b64_tr_b16 v[182:183], v51 offset:9216
	v_mfma_f32_16x16x32_f16 a[104:107], v[108:111], v[76:79], a[104:107]
	ds_read_b64_tr_b16 v[184:185], v52 offset:8192
	v_mfma_f32_16x16x32_f16 a[136:139], v[108:111], v[80:83], a[136:139]
	ds_read_b64_tr_b16 v[186:187], v52 offset:9216
	v_mfma_f32_16x16x32_f16 a[12:15], v[112:115], v[64:67], a[12:15]
	ds_read_b64_tr_b16 v[188:189], v53 offset:8192
	v_mfma_f32_16x16x32_f16 a[44:47], v[112:115], v[68:71], a[44:47]
	ds_read_b64_tr_b16 v[190:191], v53 offset:9216
	v_mfma_f32_16x16x32_f16 a[76:79], v[112:115], v[72:75], a[76:79]
	ds_read_b64_tr_b16 v[192:193], v54 offset:8192
	v_mfma_f32_16x16x32_f16 a[108:111], v[112:115], v[76:79], a[108:111]
	ds_read_b64_tr_b16 v[194:195], v54 offset:9216
	v_mfma_f32_16x16x32_f16 a[140:143], v[112:115], v[80:83], a[140:143]
	ds_read_b64_tr_b16 v[196:197], v55 offset:8192
	v_mfma_f32_16x16x32_f16 a[16:19], v[116:119], v[64:67], a[16:19]
	ds_read_b64_tr_b16 v[198:199], v55 offset:9216
	v_mfma_f32_16x16x32_f16 a[48:51], v[116:119], v[68:71], a[48:51]
	v_mfma_f32_16x16x32_f16 a[80:83], v[116:119], v[72:75], a[80:83]
	v_mfma_f32_16x16x32_f16 a[112:115], v[116:119], v[76:79], a[112:115]
	v_mfma_f32_16x16x32_f16 a[144:147], v[116:119], v[80:83], a[144:147]
	v_mfma_f32_16x16x32_f16 a[20:23], v[120:123], v[64:67], a[20:23]
	v_mfma_f32_16x16x32_f16 a[52:55], v[120:123], v[68:71], a[52:55]
	v_mfma_f32_16x16x32_f16 a[84:87], v[120:123], v[72:75], a[84:87]
	v_mfma_f32_16x16x32_f16 a[116:119], v[120:123], v[76:79], a[116:119]
	v_mfma_f32_16x16x32_f16 a[148:151], v[120:123], v[80:83], a[148:151]
	v_mfma_f32_16x16x32_f16 a[24:27], v[124:127], v[64:67], a[24:27]
	v_mfma_f32_16x16x32_f16 a[56:59], v[124:127], v[68:71], a[56:59]
	v_mfma_f32_16x16x32_f16 a[88:91], v[124:127], v[72:75], a[88:91]
	v_mfma_f32_16x16x32_f16 a[120:123], v[124:127], v[76:79], a[120:123]
	v_mfma_f32_16x16x32_f16 a[152:155], v[124:127], v[80:83], a[152:155]
	v_mfma_f32_16x16x32_f16 a[28:31], v[128:131], v[64:67], a[28:31]
	v_mfma_f32_16x16x32_f16 a[60:63], v[128:131], v[68:71], a[60:63]
	v_mfma_f32_16x16x32_f16 a[92:95], v[128:131], v[72:75], a[92:95]
	v_mfma_f32_16x16x32_f16 a[124:127], v[128:131], v[76:79], a[124:127]
	v_mfma_f32_16x16x32_f16 a[156:159], v[128:131], v[80:83], a[156:159]
	s_waitcnt lgkmcnt(0)
	v_mfma_f32_16x16x32_f16 a[0:3], v[168:171], v[132:135], a[0:3]
	v_mfma_f32_16x16x32_f16 a[32:35], v[168:171], v[136:139], a[32:35]
	v_mfma_f32_16x16x32_f16 a[64:67], v[168:171], v[140:143], a[64:67]
	v_mfma_f32_16x16x32_f16 a[96:99], v[168:171], v[144:147], a[96:99]
	v_mfma_f32_16x16x32_f16 a[128:131], v[168:171], v[148:151], a[128:131]
	v_mfma_f32_16x16x32_f16 a[4:7], v[172:175], v[132:135], a[4:7]
	v_mfma_f32_16x16x32_f16 a[36:39], v[172:175], v[136:139], a[36:39]
	v_mfma_f32_16x16x32_f16 a[68:71], v[172:175], v[140:143], a[68:71]
	v_mfma_f32_16x16x32_f16 a[100:103], v[172:175], v[144:147], a[100:103]
	v_mfma_f32_16x16x32_f16 a[132:135], v[172:175], v[148:151], a[132:135]
	v_mfma_f32_16x16x32_f16 a[8:11], v[176:179], v[132:135], a[8:11]
	v_mfma_f32_16x16x32_f16 a[40:43], v[176:179], v[136:139], a[40:43]
	v_mfma_f32_16x16x32_f16 a[72:75], v[176:179], v[140:143], a[72:75]
	v_mfma_f32_16x16x32_f16 a[104:107], v[176:179], v[144:147], a[104:107]
	v_mfma_f32_16x16x32_f16 a[136:139], v[176:179], v[148:151], a[136:139]
	v_mfma_f32_16x16x32_f16 a[12:15], v[180:183], v[132:135], a[12:15]
	v_mfma_f32_16x16x32_f16 a[44:47], v[180:183], v[136:139], a[44:47]
	v_mfma_f32_16x16x32_f16 a[76:79], v[180:183], v[140:143], a[76:79]
	v_mfma_f32_16x16x32_f16 a[108:111], v[180:183], v[144:147], a[108:111]
	v_mfma_f32_16x16x32_f16 a[140:143], v[180:183], v[148:151], a[140:143]
	v_mfma_f32_16x16x32_f16 a[16:19], v[184:187], v[132:135], a[16:19]
	v_mfma_f32_16x16x32_f16 a[48:51], v[184:187], v[136:139], a[48:51]
	v_mfma_f32_16x16x32_f16 a[80:83], v[184:187], v[140:143], a[80:83]
	v_mfma_f32_16x16x32_f16 a[112:115], v[184:187], v[144:147], a[112:115]
	v_mfma_f32_16x16x32_f16 a[144:147], v[184:187], v[148:151], a[144:147]
	v_mfma_f32_16x16x32_f16 a[20:23], v[188:191], v[132:135], a[20:23]
	v_mfma_f32_16x16x32_f16 a[52:55], v[188:191], v[136:139], a[52:55]
	v_mfma_f32_16x16x32_f16 a[84:87], v[188:191], v[140:143], a[84:87]
	v_mfma_f32_16x16x32_f16 a[116:119], v[188:191], v[144:147], a[116:119]
	v_mfma_f32_16x16x32_f16 a[148:151], v[188:191], v[148:151], a[148:151]
	v_mfma_f32_16x16x32_f16 a[24:27], v[192:195], v[132:135], a[24:27]
	v_mfma_f32_16x16x32_f16 a[56:59], v[192:195], v[136:139], a[56:59]
	v_mfma_f32_16x16x32_f16 a[88:91], v[192:195], v[140:143], a[88:91]
	v_mfma_f32_16x16x32_f16 a[120:123], v[192:195], v[144:147], a[120:123]
	v_mfma_f32_16x16x32_f16 a[152:155], v[192:195], v[148:151], a[152:155]
	v_mfma_f32_16x16x32_f16 a[28:31], v[196:199], v[132:135], a[28:31]
	v_mfma_f32_16x16x32_f16 a[60:63], v[196:199], v[136:139], a[60:63]
	v_mfma_f32_16x16x32_f16 a[92:95], v[196:199], v[140:143], a[92:95]
	v_mfma_f32_16x16x32_f16 a[124:127], v[196:199], v[144:147], a[124:127]
	v_mfma_f32_16x16x32_f16 a[156:159], v[196:199], v[148:151], a[156:159]
	s_nop 7
	s_nop 7
	s_waitcnt vmcnt(0)
	s_lshl_b32 s22, s60, 7
	s_add_i32 s22, s22, s57
	v_lshl_add_u32 v9, v4, 2, s22
	v_lshlrev_b32_e32 v9, 2, v9
	s_cmp_le_u32 s62, 0
	s_cbranch_scc1 .Lg2_epdone
	v_add_u32_e32 v8, 0, v241
	v_cmp_gt_u32_e32 vcc, s49, v8
	s_and_saveexec_b64 s[78:79], vcc
	v_lshl_add_u32 v56, v232, 12, v9
	v_accvgpr_read_b32 v244, a0
	v_accvgpr_read_b32 v245, a1
	v_accvgpr_read_b32 v246, a2
	v_accvgpr_read_b32 v247, a3
	v_add_f32_e32 v244, v244, v200
	v_add_f32_e32 v245, v245, v201
	v_add_f32_e32 v246, v246, v202
	v_add_f32_e32 v247, v247, v203
	global_store_dwordx4 v56, v[244:247], s[12:13] offset:0 sc1
	v_accvgpr_read_b32 v248, a4
	v_accvgpr_read_b32 v249, a5
	v_accvgpr_read_b32 v250, a6
	v_accvgpr_read_b32 v251, a7
	v_add_f32_e32 v248, v248, v204
	v_add_f32_e32 v249, v249, v205
	v_add_f32_e32 v250, v250, v206
	v_add_f32_e32 v251, v251, v207
	global_store_dwordx4 v56, v[248:251], s[12:13] offset:64 sc1
	v_accvgpr_read_b32 v252, a8
	v_accvgpr_read_b32 v253, a9
	v_accvgpr_read_b32 v254, a10
	v_accvgpr_read_b32 v255, a11
	v_add_f32_e32 v252, v252, v208
	v_add_f32_e32 v253, v253, v209
	v_add_f32_e32 v254, v254, v210
	v_add_f32_e32 v255, v255, v211
	global_store_dwordx4 v56, v[252:255], s[12:13] offset:128 sc1
	v_accvgpr_read_b32 v244, a12
	v_accvgpr_read_b32 v245, a13
	v_accvgpr_read_b32 v246, a14
	v_accvgpr_read_b32 v247, a15
	v_add_f32_e32 v244, v244, v212
	v_add_f32_e32 v245, v245, v213
	v_add_f32_e32 v246, v246, v214
	v_add_f32_e32 v247, v247, v215
	global_store_dwordx4 v56, v[244:247], s[12:13] offset:192 sc1
	v_accvgpr_read_b32 v248, a16
	v_accvgpr_read_b32 v249, a17
	v_accvgpr_read_b32 v250, a18
	v_accvgpr_read_b32 v251, a19
	v_add_f32_e32 v248, v248, v216
	v_add_f32_e32 v249, v249, v217
	v_add_f32_e32 v250, v250, v218
	v_add_f32_e32 v251, v251, v219
	global_store_dwordx4 v56, v[248:251], s[12:13] offset:256 sc1
	v_accvgpr_read_b32 v252, a20
	v_accvgpr_read_b32 v253, a21
	v_accvgpr_read_b32 v254, a22
	v_accvgpr_read_b32 v255, a23
	v_add_f32_e32 v252, v252, v220
	v_add_f32_e32 v253, v253, v221
	v_add_f32_e32 v254, v254, v222
	v_add_f32_e32 v255, v255, v223
	global_store_dwordx4 v56, v[252:255], s[12:13] offset:320 sc1
	v_accvgpr_read_b32 v244, a24
	v_accvgpr_read_b32 v245, a25
	v_accvgpr_read_b32 v246, a26
	v_accvgpr_read_b32 v247, a27
	v_add_f32_e32 v244, v244, v224
	v_add_f32_e32 v245, v245, v225
	v_add_f32_e32 v246, v246, v226
	v_add_f32_e32 v247, v247, v227
	global_store_dwordx4 v56, v[244:247], s[12:13] offset:384 sc1
	v_accvgpr_read_b32 v248, a28
	v_accvgpr_read_b32 v249, a29
	v_accvgpr_read_b32 v250, a30
	v_accvgpr_read_b32 v251, a31
	v_add_f32_e32 v248, v248, v228
	v_add_f32_e32 v249, v249, v229
	v_add_f32_e32 v250, v250, v230
	v_add_f32_e32 v251, v251, v231
	global_store_dwordx4 v56, v[248:251], s[12:13] offset:448 sc1
	s_mov_b64 exec, s[78:79]
	s_cmp_le_u32 s62, 1
	s_cbranch_scc1 .Lg2_epdone
	v_add_u32_e32 v8, 16, v241
	v_cmp_gt_u32_e32 vcc, s49, v8
	s_and_saveexec_b64 s[78:79], vcc
	v_lshl_add_u32 v56, v233, 12, v9
	v_accvgpr_read_b32 v252, a32
	v_accvgpr_read_b32 v253, a33
	v_accvgpr_read_b32 v254, a34
	v_accvgpr_read_b32 v255, a35
	v_add_f32_e32 v252, v252, v200
	v_add_f32_e32 v253, v253, v201
	v_add_f32_e32 v254, v254, v202
	v_add_f32_e32 v255, v255, v203
	global_store_dwordx4 v56, v[252:255], s[12:13] offset:0 sc1
	v_accvgpr_read_b32 v244, a36
	v_accvgpr_read_b32 v245, a37
	v_accvgpr_read_b32 v246, a38
	v_accvgpr_read_b32 v247, a39
	v_add_f32_e32 v244, v244, v204
	v_add_f32_e32 v245, v245, v205
	v_add_f32_e32 v246, v246, v206
	v_add_f32_e32 v247, v247, v207
	global_store_dwordx4 v56, v[244:247], s[12:13] offset:64 sc1
	v_accvgpr_read_b32 v248, a40
	v_accvgpr_read_b32 v249, a41
	v_accvgpr_read_b32 v250, a42
	v_accvgpr_read_b32 v251, a43
	v_add_f32_e32 v248, v248, v208
	v_add_f32_e32 v249, v249, v209
	v_add_f32_e32 v250, v250, v210
	v_add_f32_e32 v251, v251, v211
	global_store_dwordx4 v56, v[248:251], s[12:13] offset:128 sc1
	v_accvgpr_read_b32 v252, a44
	v_accvgpr_read_b32 v253, a45
	v_accvgpr_read_b32 v254, a46
	v_accvgpr_read_b32 v255, a47
	v_add_f32_e32 v252, v252, v212
	v_add_f32_e32 v253, v253, v213
	v_add_f32_e32 v254, v254, v214
	v_add_f32_e32 v255, v255, v215
	global_store_dwordx4 v56, v[252:255], s[12:13] offset:192 sc1
	v_accvgpr_read_b32 v244, a48
	v_accvgpr_read_b32 v245, a49
	v_accvgpr_read_b32 v246, a50
	v_accvgpr_read_b32 v247, a51
	v_add_f32_e32 v244, v244, v216
	v_add_f32_e32 v245, v245, v217
	v_add_f32_e32 v246, v246, v218
	v_add_f32_e32 v247, v247, v219
	global_store_dwordx4 v56, v[244:247], s[12:13] offset:256 sc1
	v_accvgpr_read_b32 v248, a52
	v_accvgpr_read_b32 v249, a53
	v_accvgpr_read_b32 v250, a54
	v_accvgpr_read_b32 v251, a55
	v_add_f32_e32 v248, v248, v220
	v_add_f32_e32 v249, v249, v221
	v_add_f32_e32 v250, v250, v222
	v_add_f32_e32 v251, v251, v223
	global_store_dwordx4 v56, v[248:251], s[12:13] offset:320 sc1
	v_accvgpr_read_b32 v252, a56
	v_accvgpr_read_b32 v253, a57
	v_accvgpr_read_b32 v254, a58
	v_accvgpr_read_b32 v255, a59
	v_add_f32_e32 v252, v252, v224
	v_add_f32_e32 v253, v253, v225
	v_add_f32_e32 v254, v254, v226
	v_add_f32_e32 v255, v255, v227
	global_store_dwordx4 v56, v[252:255], s[12:13] offset:384 sc1
	v_accvgpr_read_b32 v244, a60
	v_accvgpr_read_b32 v245, a61
	v_accvgpr_read_b32 v246, a62
	v_accvgpr_read_b32 v247, a63
	v_add_f32_e32 v244, v244, v228
	v_add_f32_e32 v245, v245, v229
	v_add_f32_e32 v246, v246, v230
	v_add_f32_e32 v247, v247, v231
	global_store_dwordx4 v56, v[244:247], s[12:13] offset:448 sc1
	s_mov_b64 exec, s[78:79]
	s_cmp_le_u32 s62, 2
	s_cbranch_scc1 .Lg2_epdone
	v_add_u32_e32 v8, 32, v241
	v_cmp_gt_u32_e32 vcc, s49, v8
	s_and_saveexec_b64 s[78:79], vcc
	v_lshl_add_u32 v56, v234, 12, v9
	v_accvgpr_read_b32 v248, a64
	v_accvgpr_read_b32 v249, a65
	v_accvgpr_read_b32 v250, a66
	v_accvgpr_read_b32 v251, a67
	v_add_f32_e32 v248, v248, v200
	v_add_f32_e32 v249, v249, v201
	v_add_f32_e32 v250, v250, v202
	v_add_f32_e32 v251, v251, v203
	global_store_dwordx4 v56, v[248:251], s[12:13] offset:0 sc1
	v_accvgpr_read_b32 v252, a68
	v_accvgpr_read_b32 v253, a69
	v_accvgpr_read_b32 v254, a70
	v_accvgpr_read_b32 v255, a71
	v_add_f32_e32 v252, v252, v204
	v_add_f32_e32 v253, v253, v205
	v_add_f32_e32 v254, v254, v206
	v_add_f32_e32 v255, v255, v207
	global_store_dwordx4 v56, v[252:255], s[12:13] offset:64 sc1
	v_accvgpr_read_b32 v244, a72
	v_accvgpr_read_b32 v245, a73
	v_accvgpr_read_b32 v246, a74
	v_accvgpr_read_b32 v247, a75
	v_add_f32_e32 v244, v244, v208
	v_add_f32_e32 v245, v245, v209
	v_add_f32_e32 v246, v246, v210
	v_add_f32_e32 v247, v247, v211
	global_store_dwordx4 v56, v[244:247], s[12:13] offset:128 sc1
	v_accvgpr_read_b32 v248, a76
	v_accvgpr_read_b32 v249, a77
	v_accvgpr_read_b32 v250, a78
	v_accvgpr_read_b32 v251, a79
	v_add_f32_e32 v248, v248, v212
	v_add_f32_e32 v249, v249, v213
	v_add_f32_e32 v250, v250, v214
	v_add_f32_e32 v251, v251, v215
	global_store_dwordx4 v56, v[248:251], s[12:13] offset:192 sc1
	v_accvgpr_read_b32 v252, a80
	v_accvgpr_read_b32 v253, a81
	v_accvgpr_read_b32 v254, a82
	v_accvgpr_read_b32 v255, a83
	v_add_f32_e32 v252, v252, v216
	v_add_f32_e32 v253, v253, v217
	v_add_f32_e32 v254, v254, v218
	v_add_f32_e32 v255, v255, v219
	global_store_dwordx4 v56, v[252:255], s[12:13] offset:256 sc1
	v_accvgpr_read_b32 v244, a84
	v_accvgpr_read_b32 v245, a85
	v_accvgpr_read_b32 v246, a86
	v_accvgpr_read_b32 v247, a87
	v_add_f32_e32 v244, v244, v220
	v_add_f32_e32 v245, v245, v221
	v_add_f32_e32 v246, v246, v222
	v_add_f32_e32 v247, v247, v223
	global_store_dwordx4 v56, v[244:247], s[12:13] offset:320 sc1
	v_accvgpr_read_b32 v248, a88
	v_accvgpr_read_b32 v249, a89
	v_accvgpr_read_b32 v250, a90
	v_accvgpr_read_b32 v251, a91
	v_add_f32_e32 v248, v248, v224
	v_add_f32_e32 v249, v249, v225
	v_add_f32_e32 v250, v250, v226
	v_add_f32_e32 v251, v251, v227
	global_store_dwordx4 v56, v[248:251], s[12:13] offset:384 sc1
	v_accvgpr_read_b32 v252, a92
	v_accvgpr_read_b32 v253, a93
	v_accvgpr_read_b32 v254, a94
	v_accvgpr_read_b32 v255, a95
	v_add_f32_e32 v252, v252, v228
	v_add_f32_e32 v253, v253, v229
	v_add_f32_e32 v254, v254, v230
	v_add_f32_e32 v255, v255, v231
	global_store_dwordx4 v56, v[252:255], s[12:13] offset:448 sc1
	s_mov_b64 exec, s[78:79]
	s_cmp_le_u32 s62, 3
	s_cbranch_scc1 .Lg2_epdone
	v_add_u32_e32 v8, 48, v241
	v_cmp_gt_u32_e32 vcc, s49, v8
	s_and_saveexec_b64 s[78:79], vcc
	v_lshl_add_u32 v56, v235, 12, v9
	v_accvgpr_read_b32 v244, a96
	v_accvgpr_read_b32 v245, a97
	v_accvgpr_read_b32 v246, a98
	v_accvgpr_read_b32 v247, a99
	v_add_f32_e32 v244, v244, v200
	v_add_f32_e32 v245, v245, v201
	v_add_f32_e32 v246, v246, v202
	v_add_f32_e32 v247, v247, v203
	global_store_dwordx4 v56, v[244:247], s[12:13] offset:0 sc1
	v_accvgpr_read_b32 v248, a100
	v_accvgpr_read_b32 v249, a101
	v_accvgpr_read_b32 v250, a102
	v_accvgpr_read_b32 v251, a103
	v_add_f32_e32 v248, v248, v204
	v_add_f32_e32 v249, v249, v205
	v_add_f32_e32 v250, v250, v206
	v_add_f32_e32 v251, v251, v207
	global_store_dwordx4 v56, v[248:251], s[12:13] offset:64 sc1
	v_accvgpr_read_b32 v252, a104
	v_accvgpr_read_b32 v253, a105
	v_accvgpr_read_b32 v254, a106
	v_accvgpr_read_b32 v255, a107
	v_add_f32_e32 v252, v252, v208
	v_add_f32_e32 v253, v253, v209
	v_add_f32_e32 v254, v254, v210
	v_add_f32_e32 v255, v255, v211
	global_store_dwordx4 v56, v[252:255], s[12:13] offset:128 sc1
	v_accvgpr_read_b32 v244, a108
	v_accvgpr_read_b32 v245, a109
	v_accvgpr_read_b32 v246, a110
	v_accvgpr_read_b32 v247, a111
	v_add_f32_e32 v244, v244, v212
	v_add_f32_e32 v245, v245, v213
	v_add_f32_e32 v246, v246, v214
	v_add_f32_e32 v247, v247, v215
	global_store_dwordx4 v56, v[244:247], s[12:13] offset:192 sc1
	v_accvgpr_read_b32 v248, a112
	v_accvgpr_read_b32 v249, a113
	v_accvgpr_read_b32 v250, a114
	v_accvgpr_read_b32 v251, a115
	v_add_f32_e32 v248, v248, v216
	v_add_f32_e32 v249, v249, v217
	v_add_f32_e32 v250, v250, v218
	v_add_f32_e32 v251, v251, v219
	global_store_dwordx4 v56, v[248:251], s[12:13] offset:256 sc1
	v_accvgpr_read_b32 v252, a116
	v_accvgpr_read_b32 v253, a117
	v_accvgpr_read_b32 v254, a118
	v_accvgpr_read_b32 v255, a119
	v_add_f32_e32 v252, v252, v220
	v_add_f32_e32 v253, v253, v221
	v_add_f32_e32 v254, v254, v222
	v_add_f32_e32 v255, v255, v223
	global_store_dwordx4 v56, v[252:255], s[12:13] offset:320 sc1
	v_accvgpr_read_b32 v244, a120
	v_accvgpr_read_b32 v245, a121
	v_accvgpr_read_b32 v246, a122
	v_accvgpr_read_b32 v247, a123
	v_add_f32_e32 v244, v244, v224
	v_add_f32_e32 v245, v245, v225
	v_add_f32_e32 v246, v246, v226
	v_add_f32_e32 v247, v247, v227
	global_store_dwordx4 v56, v[244:247], s[12:13] offset:384 sc1
	v_accvgpr_read_b32 v248, a124
	v_accvgpr_read_b32 v249, a125
	v_accvgpr_read_b32 v250, a126
	v_accvgpr_read_b32 v251, a127
	v_add_f32_e32 v248, v248, v228
	v_add_f32_e32 v249, v249, v229
	v_add_f32_e32 v250, v250, v230
	v_add_f32_e32 v251, v251, v231
	global_store_dwordx4 v56, v[248:251], s[12:13] offset:448 sc1
	s_mov_b64 exec, s[78:79]
	s_cmp_le_u32 s62, 4
	s_cbranch_scc1 .Lg2_epdone
	v_add_u32_e32 v8, 64, v241
	v_cmp_gt_u32_e32 vcc, s49, v8
	s_and_saveexec_b64 s[78:79], vcc
	v_lshl_add_u32 v56, v236, 12, v9
	v_accvgpr_read_b32 v252, a128
	v_accvgpr_read_b32 v253, a129
	v_accvgpr_read_b32 v254, a130
	v_accvgpr_read_b32 v255, a131
	v_add_f32_e32 v252, v252, v200
	v_add_f32_e32 v253, v253, v201
	v_add_f32_e32 v254, v254, v202
	v_add_f32_e32 v255, v255, v203
	global_store_dwordx4 v56, v[252:255], s[12:13] offset:0 sc1
	v_accvgpr_read_b32 v244, a132
	v_accvgpr_read_b32 v245, a133
	v_accvgpr_read_b32 v246, a134
	v_accvgpr_read_b32 v247, a135
	v_add_f32_e32 v244, v244, v204
	v_add_f32_e32 v245, v245, v205
	v_add_f32_e32 v246, v246, v206
	v_add_f32_e32 v247, v247, v207
	global_store_dwordx4 v56, v[244:247], s[12:13] offset:64 sc1
	v_accvgpr_read_b32 v248, a136
	v_accvgpr_read_b32 v249, a137
	v_accvgpr_read_b32 v250, a138
	v_accvgpr_read_b32 v251, a139
	v_add_f32_e32 v248, v248, v208
	v_add_f32_e32 v249, v249, v209
	v_add_f32_e32 v250, v250, v210
	v_add_f32_e32 v251, v251, v211
	global_store_dwordx4 v56, v[248:251], s[12:13] offset:128 sc1
	v_accvgpr_read_b32 v252, a140
	v_accvgpr_read_b32 v253, a141
	v_accvgpr_read_b32 v254, a142
	v_accvgpr_read_b32 v255, a143
	v_add_f32_e32 v252, v252, v212
	v_add_f32_e32 v253, v253, v213
	v_add_f32_e32 v254, v254, v214
	v_add_f32_e32 v255, v255, v215
	global_store_dwordx4 v56, v[252:255], s[12:13] offset:192 sc1
	v_accvgpr_read_b32 v244, a144
	v_accvgpr_read_b32 v245, a145
	v_accvgpr_read_b32 v246, a146
	v_accvgpr_read_b32 v247, a147
	v_add_f32_e32 v244, v244, v216
	v_add_f32_e32 v245, v245, v217
	v_add_f32_e32 v246, v246, v218
	v_add_f32_e32 v247, v247, v219
	global_store_dwordx4 v56, v[244:247], s[12:13] offset:256 sc1
	v_accvgpr_read_b32 v248, a148
	v_accvgpr_read_b32 v249, a149
	v_accvgpr_read_b32 v250, a150
	v_accvgpr_read_b32 v251, a151
	v_add_f32_e32 v248, v248, v220
	v_add_f32_e32 v249, v249, v221
	v_add_f32_e32 v250, v250, v222
	v_add_f32_e32 v251, v251, v223
	global_store_dwordx4 v56, v[248:251], s[12:13] offset:320 sc1
	v_accvgpr_read_b32 v252, a152
	v_accvgpr_read_b32 v253, a153
	v_accvgpr_read_b32 v254, a154
	v_accvgpr_read_b32 v255, a155
	v_add_f32_e32 v252, v252, v224
	v_add_f32_e32 v253, v253, v225
	v_add_f32_e32 v254, v254, v226
	v_add_f32_e32 v255, v255, v227
	global_store_dwordx4 v56, v[252:255], s[12:13] offset:384 sc1
	v_accvgpr_read_b32 v244, a156
	v_accvgpr_read_b32 v245, a157
	v_accvgpr_read_b32 v246, a158
	v_accvgpr_read_b32 v247, a159
	v_add_f32_e32 v244, v244, v228
	v_add_f32_e32 v245, v245, v229
	v_add_f32_e32 v246, v246, v230
	v_add_f32_e32 v247, v247, v231
	global_store_dwordx4 v56, v[244:247], s[12:13] offset:448 sc1
	s_mov_b64 exec, s[78:79]
.Lg2_epdone:
	s_add_i32 s18, s18, s20
	s_cmp_lt_i32 s18, s19
	s_cbranch_scc1 .Lg2_tile

	.amdhsa_kernel _Z8moe_gemmILi2048ELi1024ELb0EEvPKDF16_S1_PKfPDF16_PfPKiS7_
		.amdhsa_group_segment_fixed_size 86016
		.amdhsa_private_segment_fixed_size 0
		.amdhsa_kernarg_size 312
		.amdhsa_user_sgpr_count 2
		.amdhsa_user_sgpr_dispatch_ptr 0
		.amdhsa_user_sgpr_queue_ptr 0
		.amdhsa_user_sgpr_kernarg_segment_ptr 1
		.amdhsa_user_sgpr_dispatch_id 0
		.amdhsa_user_sgpr_kernarg_preload_length 0
		.amdhsa_user_sgpr_kernarg_preload_offset 0
		.amdhsa_user_sgpr_private_segment_size 0
		.amdhsa_uses_dynamic_stack 0
		.amdhsa_enable_private_segment 0
		.amdhsa_system_sgpr_workgroup_id_x 1
		.amdhsa_system_sgpr_workgroup_id_y 0
		.amdhsa_system_sgpr_workgroup_id_z 0
		.amdhsa_system_sgpr_workgroup_info 0
		.amdhsa_system_vgpr_workitem_id 0
		.amdhsa_next_free_vgpr 512
		.amdhsa_next_free_sgpr 90
		.amdhsa_accum_offset 256
		.amdhsa_reserve_vcc 1
		.amdhsa_float_round_mode_32 0
		.amdhsa_float_round_mode_16_64 0
		.amdhsa_float_denorm_mode_32 3
		.amdhsa_float_denorm_mode_16_64 3
		.amdhsa_dx10_clamp 1
		.amdhsa_ieee_mode 1
		.amdhsa_fp16_overflow 0
		.amdhsa_tg_split 0
		.amdhsa_exception_fp_ieee_invalid_op 0
		.amdhsa_exception_fp_denorm_src 0
		.amdhsa_exception_fp_ieee_div_zero 0
		.amdhsa_exception_fp_ieee_overflow 0
		.amdhsa_exception_fp_ieee_underflow 0
		.amdhsa_exception_fp_ieee_inexact 0
		.amdhsa_exception_int_div_zero 0
	.end_amdhsa_kernel

	.text
	.p2alignl 6, 3212836864
	.fill 256, 4, 3212836864
	.p2align	8

amdhsa.kernels:
  - .agpr_count:     0
    .args:
      - .actual_access:  read_only
        .address_space:  global
        .offset:         0
        .size:           8
        .value_kind:     global_buffer
      - .address_space:  global
        .offset:         8
        .size:           8
        .value_kind:     global_buffer
      - .actual_access:  read_only
        .address_space:  global
        .offset:         16
        .size:           8
        .value_kind:     global_buffer
      - .address_space:  global
        .offset:         24
        .size:           8
        .value_kind:     global_buffer
      - .offset:         32
        .size:           4
        .value_kind:     by_value
      - .actual_access:  write_only
        .address_space:  global
        .offset:         40
        .size:           8
        .value_kind:     global_buffer
      - .offset:         48
        .size:           4
        .value_kind:     hidden_block_count_x
      - .offset:         52
        .size:           4
        .value_kind:     hidden_block_count_y
      - .offset:         56
        .size:           4
        .value_kind:     hidden_block_count_z
      - .offset:         60
        .size:           2
        .value_kind:     hidden_group_size_x
      - .offset:         62
        .size:           2
        .value_kind:     hidden_group_size_y
      - .offset:         64
        .size:           2
        .value_kind:     hidden_group_size_z
      - .offset:         66
        .size:           2
        .value_kind:     hidden_remainder_x
      - .offset:         68
        .size:           2
        .value_kind:     hidden_remainder_y
      - .offset:         70
        .size:           2
        .value_kind:     hidden_remainder_z
      - .offset:         88
        .size:           8
        .value_kind:     hidden_global_offset_x
      - .offset:         96
        .size:           8
        .value_kind:     hidden_global_offset_y
      - .offset:         104
        .size:           8
        .value_kind:     hidden_global_offset_z
      - .offset:         112
        .size:           2
        .value_kind:     hidden_grid_dims
    .group_segment_fixed_size: 0
    .kernarg_segment_align: 8
    .kernarg_segment_size: 304
    .language:       OpenCL C
    .language_version:
      - 2
      - 0
    .max_flat_workgroup_size: 256
    .name:           _Z5cvt_wPKfPDF16_S0_S1_iPi
    .private_segment_fixed_size: 0
    .sgpr_count:     22
    .sgpr_spill_count: 0
    .symbol:         _Z5cvt_wPKfPDF16_S0_S1_iPi.kd
    .uniform_work_group_size: 1
    .uses_dynamic_stack: false
    .vgpr_count:     22
    .vgpr_spill_count: 0
    .wavefront_size: 64
  - .agpr_count:     0
    .args:
      - .actual_access:  read_only
        .address_space:  global
        .offset:         0
        .size:           8
        .value_kind:     global_buffer
      - .actual_access:  read_only
        .address_space:  global
        .offset:         8
        .size:           8
        .value_kind:     global_buffer
      - .actual_access:  read_only
        .address_space:  global
        .offset:         16
        .size:           8
        .value_kind:     global_buffer
      - .actual_access:  write_only
        .address_space:  global
        .offset:         24
        .size:           8
        .value_kind:     global_buffer
      - .address_space:  global
        .offset:         32
        .size:           8
        .value_kind:     global_buffer
      - .actual_access:  write_only
        .address_space:  global
        .offset:         40
        .size:           8
        .value_kind:     global_buffer
      - .actual_access:  write_only
        .address_space:  global
        .offset:         48
        .size:           8
        .value_kind:     global_buffer
      - .actual_access:  read_only
        .address_space:  global
        .offset:         56
        .size:           8
        .value_kind:     global_buffer
      - .address_space:  global
        .offset:         64
        .size:           8
        .value_kind:     global_buffer
      - .offset:         72
        .size:           4
        .value_kind:     by_value
      - .offset:         80
        .size:           4
        .value_kind:     hidden_block_count_x
      - .offset:         84
        .size:           4
        .value_kind:     hidden_block_count_y
      - .offset:         88
        .size:           4
        .value_kind:     hidden_block_count_z
      - .offset:         92
        .size:           2
        .value_kind:     hidden_group_size_x
      - .offset:         94
        .size:           2
        .value_kind:     hidden_group_size_y
      - .offset:         96
        .size:           2
        .value_kind:     hidden_group_size_z
      - .offset:         98
        .size:           2
        .value_kind:     hidden_remainder_x
      - .offset:         100
        .size:           2
        .value_kind:     hidden_remainder_y
      - .offset:         102
        .size:           2
        .value_kind:     hidden_remainder_z
      - .offset:         120
        .size:           8
        .value_kind:     hidden_global_offset_x
      - .offset:         128
        .size:           8
        .value_kind:     hidden_global_offset_y
      - .offset:         136
        .size:           8
        .value_kind:     hidden_global_offset_z
      - .offset:         144
        .size:           2
        .value_kind:     hidden_grid_dims
    .group_segment_fixed_size: 32928
    .kernarg_segment_align: 8
    .kernarg_segment_size: 336
    .language:       OpenCL C
    .language_version:
      - 2
      - 0
    .max_flat_workgroup_size: 512
    .name:           _Z11gate_kernelPKfS0_S0_PDF16_PiS2_PfS0_S1_i
    .private_segment_fixed_size: 0
    .sgpr_count:     66
    .sgpr_spill_count: 0
    .symbol:         _Z11gate_kernelPKfS0_S0_PDF16_PiS2_PfS0_S1_i.kd
    .uniform_work_group_size: 1
    .uses_dynamic_stack: false
    .vgpr_count:     115
    .vgpr_spill_count: 0
    .wavefront_size: 64
  - .agpr_count:     0
    .args:
      - .address_space:  global
        .offset:         0
        .size:           8
        .value_kind:     global_buffer
      - .address_space:  global
        .offset:         8
        .size:           8
        .value_kind:     global_buffer
      - .actual_access:  read_only
        .address_space:  global
        .offset:         16
        .size:           8
        .value_kind:     global_buffer
      - .address_space:  global
        .offset:         24
        .size:           8
        .value_kind:     global_buffer
      - .actual_access:  read_only
        .address_space:  global
        .offset:         32
        .size:           8
        .value_kind:     global_buffer
      - .actual_access:  read_only
        .address_space:  global
        .offset:         40
        .size:           8
        .value_kind:     global_buffer
      - .actual_access:  read_only
        .address_space:  global
        .offset:         48
        .size:           8
        .value_kind:     global_buffer
      - .offset:         56
        .size:           4
        .value_kind:     hidden_block_count_x
      - .offset:         60
        .size:           4
        .value_kind:     hidden_block_count_y
      - .offset:         64
        .size:           4
        .value_kind:     hidden_block_count_z
      - .offset:         68
        .size:           2
        .value_kind:     hidden_group_size_x
      - .offset:         70
        .size:           2
        .value_kind:     hidden_group_size_y
      - .offset:         72
        .size:           2
        .value_kind:     hidden_group_size_z
      - .offset:         74
        .size:           2
        .value_kind:     hidden_remainder_x
      - .offset:         76
        .size:           2
        .value_kind:     hidden_remainder_y
      - .offset:         78
        .size:           2
        .value_kind:     hidden_remainder_z
      - .offset:         96
        .size:           8
        .value_kind:     hidden_global_offset_x
      - .offset:         104
        .size:           8
        .value_kind:     hidden_global_offset_y
      - .offset:         112
        .size:           8
        .value_kind:     hidden_global_offset_z
      - .offset:         120
        .size:           2
        .value_kind:     hidden_grid_dims
      - .offset:         176
        .size:           4
        .value_kind:     hidden_dynamic_lds_size
    .group_segment_fixed_size: 0
    .kernarg_segment_align: 8
    .kernarg_segment_size: 312
    .language:       OpenCL C
    .language_version:
      - 2
      - 0
    .max_flat_workgroup_size: 256
    .name:           _Z8moe_gemmILi1024ELi2048ELb1EEvPKDF16_S1_PKfPDF16_PfPKiS7_
    .private_segment_fixed_size: 0
    .sgpr_count:     93
    .sgpr_spill_count: 0
    .symbol:         _Z8moe_gemmILi1024ELi2048ELb1EEvPKDF16_S1_PKfPDF16_PfPKiS7_.kd
    .uniform_work_group_size: 1
    .uses_dynamic_stack: false
    .vgpr_count:     206
    .vgpr_spill_count: 0
    .wavefront_size: 64
  - .agpr_count:     256
    .args:
      - .address_space:  global
        .offset:         0
        .size:           8
        .value_kind:     global_buffer
      - .address_space:  global
        .offset:         8
        .size:           8
        .value_kind:     global_buffer
      - .actual_access:  read_only
        .address_space:  global
        .offset:         16
        .size:           8
        .value_kind:     global_buffer
      - .actual_access:  read_only
        .address_space:  global
        .offset:         24
        .size:           8
        .value_kind:     global_buffer
      - .address_space:  global
        .offset:         32
        .size:           8
        .value_kind:     global_buffer
      - .actual_access:  read_only
        .address_space:  global
        .offset:         40
        .size:           8
        .value_kind:     global_buffer
      - .actual_access:  read_only
        .address_space:  global
        .offset:         48
        .size:           8
        .value_kind:     global_buffer
      - .offset:         56
        .size:           4
        .value_kind:     hidden_block_count_x
      - .offset:         60
        .size:           4
        .value_kind:     hidden_block_count_y
      - .offset:         64
        .size:           4
        .value_kind:     hidden_block_count_z
      - .offset:         68
        .size:           2
        .value_kind:     hidden_group_size_x
      - .offset:         70
        .size:           2
        .value_kind:     hidden_group_size_y
      - .offset:         72
        .size:           2
        .value_kind:     hidden_group_size_z
      - .offset:         74
        .size:           2
        .value_kind:     hidden_remainder_x
      - .offset:         76
        .size:           2
        .value_kind:     hidden_remainder_y
      - .offset:         78
        .size:           2
        .value_kind:     hidden_remainder_z
      - .offset:         96
        .size:           8
        .value_kind:     hidden_global_offset_x
      - .offset:         104
        .size:           8
        .value_kind:     hidden_global_offset_y
      - .offset:         112
        .size:           8
        .value_kind:     hidden_global_offset_z
      - .offset:         120
        .size:           2
        .value_kind:     hidden_grid_dims
      - .offset:         176
        .size:           4
        .value_kind:     hidden_dynamic_lds_size
    .group_segment_fixed_size: 86016
    .kernarg_segment_align: 8
    .kernarg_segment_size: 312
    .language:       OpenCL C
    .language_version:
      - 2
      - 0
    .max_flat_workgroup_size: 256
    .name:           _Z8moe_gemmILi2048ELi1024ELb0EEvPKDF16_S1_PKfPDF16_PfPKiS7_
    .private_segment_fixed_size: 0
    .sgpr_count:     96
    .sgpr_spill_count: 0
    .symbol:         _Z8moe_gemmILi2048ELi1024ELb0EEvPKDF16_S1_PKfPDF16_PfPKiS7_.kd
    .uniform_work_group_size: 1
    .uses_dynamic_stack: false
    .vgpr_count:     512
    .vgpr_spill_count: 0
    .wavefront_size: 64
